# top-k descent: per-step count split between v_addc and s_bcnt1+s_add so both waves of a SIMD co-issue
# baseline (speedup 1.0000x reference)
.Ltk0_l32:
	s_or_b32 s6, s4, s5
	v_cmp_le_u32_e64 s[10:11], s6, v172
	v_cmp_le_u32_e64 s[8:9], s6, v179
	v_cmp_le_u32_e64 s[14:15], s6, v181
	s_bcnt1_i32_b64 s28, s[10:11]
	v_cndmask_b32_e64 v8, 0, 1, s[8:9]
	s_bcnt1_i32_b64 s29, s[14:15]
	v_cmp_le_u32_e64 s[12:13], s6, v183
	s_add_u32 s28, s28, s29
	v_cmp_le_u32_e64 s[34:35], s6, v185
	v_addc_co_u32_e64 v8, s[20:21], 0, v8, s[12:13]
	v_cmp_le_u32_e64 s[10:11], s6, v187
	s_bcnt1_i32_b64 s30, s[34:35]
	v_cmp_le_u32_e64 s[16:17], s6, v189
	s_add_u32 s28, s28, s30
	v_cmp_le_u32_e64 s[14:15], s6, v190
	s_bcnt1_i32_b64 s31, s[10:11]
	v_addc_co_u32_e64 v8, s[20:21], 0, v8, s[16:17]
	s_add_u32 s28, s28, s31
	v_cmp_le_u32_e64 s[8:9], s6, v191
	s_bcnt1_i32_b64 s29, s[14:15]
	v_cmp_le_u32_e64 s[34:35], s6, v192
	s_add_u32 s28, s28, s29
	v_addc_co_u32_e64 v8, s[20:21], 0, v8, s[8:9]
	s_bcnt1_i32_b64 s30, s[34:35]
	v_cmp_le_u32_e64 s[10:11], s6, v193
	s_add_u32 s28, s28, s30
	v_cmp_le_u32_e64 s[12:13], s6, v194
	s_bcnt1_i32_b64 s31, s[10:11]
	v_cmp_le_u32_e64 s[14:15], s6, v195
	s_add_u32 s28, s28, s31
	v_addc_co_u32_e64 v8, s[20:21], 0, v8, s[12:13]
	s_bcnt1_i32_b64 s29, s[14:15]
	v_cmp_le_u32_e64 s[16:17], s6, v196
	s_add_u32 s28, s28, s29
	v_cmp_le_u32_e64 s[34:35], s6, v198
	v_addc_co_u32_e64 v8, s[20:21], 0, v8, s[16:17]
	v_cmp_le_u32_e64 s[10:11], s6, v200
	s_bcnt1_i32_b64 s30, s[34:35]
	v_cmp_le_u32_e64 s[8:9], s6, v206
	s_add_u32 s28, s28, s30
	v_cmp_le_u32_e64 s[14:15], s6, v207
	s_bcnt1_i32_b64 s31, s[10:11]
	v_addc_co_u32_e64 v8, s[20:21], 0, v8, s[8:9]
	s_add_u32 s28, s28, s31
	v_cmp_le_u32_e64 s[12:13], s6, v208
	s_bcnt1_i32_b64 s29, s[14:15]
	v_cmp_le_u32_e64 s[34:35], s6, v209
	s_add_u32 s28, s28, s29
	v_addc_co_u32_e64 v8, s[20:21], 0, v8, s[12:13]
	s_bcnt1_i32_b64 s30, s[34:35]
	v_cmp_le_u32_e64 s[10:11], s6, v210
	s_add_u32 s28, s28, s30
	v_cmp_le_u32_e64 s[16:17], s6, v211
	s_bcnt1_i32_b64 s31, s[10:11]
	v_cmp_le_u32_e64 s[14:15], s6, v212
	s_add_u32 s28, s28, s31
	v_addc_co_u32_e64 v8, s[20:21], 0, v8, s[16:17]
	s_bcnt1_i32_b64 s29, s[14:15]
	v_cmp_le_u32_e64 s[8:9], s6, v213
	s_add_u32 s28, s28, s29
	v_cmp_le_u32_e64 s[34:35], s6, v214
	v_addc_co_u32_e64 v8, s[20:21], 0, v8, s[8:9]
	v_cmp_le_u32_e64 s[10:11], s6, v215
	s_bcnt1_i32_b64 s30, s[34:35]
	v_cmp_le_u32_e64 s[12:13], s6, v216
	s_add_u32 s28, s28, s30
	v_cmp_le_u32_e64 s[14:15], s6, v217
	s_bcnt1_i32_b64 s31, s[10:11]
	v_addc_co_u32_e64 v8, s[20:21], 0, v8, s[12:13]
	s_add_u32 s28, s28, s31
	v_cmp_le_u32_e64 s[16:17], s6, v219
	s_bcnt1_i32_b64 s29, s[14:15]
	v_cmp_le_u32_e64 s[34:35], s6, v220
	s_add_u32 s28, s28, s29
	v_addc_co_u32_e64 v8, s[20:21], 0, v8, s[16:17]
	s_bcnt1_i32_b64 s30, s[34:35]
	v_cmp_le_u32_e64 s[10:11], s6, v221
	s_add_u32 s28, s28, s30
	v_cmp_le_u32_e64 s[8:9], s6, v2
	s_bcnt1_i32_b64 s31, s[10:11]
	s_add_u32 s28, s28, s31
	v_addc_co_u32_e64 v8, s[20:21], 0, v8, s[8:9]
	v_and_b32_e32 v9, 8, v8
	v_cmp_ne_u32_e64 s[18:19], 0, v9
	v_and_b32_e32 v9, 4, v8
	v_cmp_ne_u32_e64 s[16:17], 0, v9
	v_and_b32_e32 v9, 2, v8
	v_cmp_ne_u32_e64 s[12:13], 0, v9
	v_and_b32_e32 v9, 1, v8
	v_cmp_ne_u32_e64 s[8:9], 0, v9
	s_bcnt1_i32_b64 s7, s[18:19]
	s_bcnt1_i32_b64 s3, s[16:17]
	s_lshl1_add_u32 s7, s7, s3
	s_bcnt1_i32_b64 s3, s[12:13]
	s_lshl1_add_u32 s7, s7, s3
	s_bcnt1_i32_b64 s3, s[8:9]
	s_lshl1_add_u32 s7, s7, s3
	s_add_u32 s7, s7, s28
	s_cmpk_lt_u32 s7, 0x100
	s_cselect_b32 s4, s4, s6
	s_cmpk_eq_u32 s7, 0x100
	s_cbranch_scc1 .Ltk0_x32
	s_lshr_b32 s5, s5, 1
	s_cbranch_scc1 .Ltk0_l32
	s_branch .Ltk0_orig
.Ltk0_l28:
	s_or_b32 s6, s4, s5
	v_cmp_le_u32_e64 s[10:11], s6, v172
	v_cmp_le_u32_e64 s[8:9], s6, v179
	v_cmp_le_u32_e64 s[14:15], s6, v181
	s_bcnt1_i32_b64 s28, s[10:11]
	v_cndmask_b32_e64 v8, 0, 1, s[8:9]
	s_bcnt1_i32_b64 s29, s[14:15]
	v_cmp_le_u32_e64 s[12:13], s6, v183
	s_add_u32 s28, s28, s29
	v_cmp_le_u32_e64 s[34:35], s6, v185
	v_addc_co_u32_e64 v8, s[20:21], 0, v8, s[12:13]
	v_cmp_le_u32_e64 s[10:11], s6, v187
	s_bcnt1_i32_b64 s30, s[34:35]
	v_cmp_le_u32_e64 s[16:17], s6, v189
	s_add_u32 s28, s28, s30
	v_cmp_le_u32_e64 s[14:15], s6, v190
	s_bcnt1_i32_b64 s31, s[10:11]
	v_addc_co_u32_e64 v8, s[20:21], 0, v8, s[16:17]
	s_add_u32 s28, s28, s31
	v_cmp_le_u32_e64 s[8:9], s6, v191
	s_bcnt1_i32_b64 s29, s[14:15]
	v_cmp_le_u32_e64 s[34:35], s6, v192
	s_add_u32 s28, s28, s29
	v_addc_co_u32_e64 v8, s[20:21], 0, v8, s[8:9]
	s_bcnt1_i32_b64 s30, s[34:35]
	v_cmp_le_u32_e64 s[10:11], s6, v193
	s_add_u32 s28, s28, s30
	v_cmp_le_u32_e64 s[12:13], s6, v194
	s_bcnt1_i32_b64 s31, s[10:11]
	v_cmp_le_u32_e64 s[14:15], s6, v195
	s_add_u32 s28, s28, s31
	v_addc_co_u32_e64 v8, s[20:21], 0, v8, s[12:13]
	s_bcnt1_i32_b64 s29, s[14:15]
	v_cmp_le_u32_e64 s[16:17], s6, v196
	s_add_u32 s28, s28, s29
	v_cmp_le_u32_e64 s[34:35], s6, v198
	v_addc_co_u32_e64 v8, s[20:21], 0, v8, s[16:17]
	v_cmp_le_u32_e64 s[10:11], s6, v200
	s_bcnt1_i32_b64 s30, s[34:35]
	v_cmp_le_u32_e64 s[8:9], s6, v206
	s_add_u32 s28, s28, s30
	v_cmp_le_u32_e64 s[14:15], s6, v207
	s_bcnt1_i32_b64 s31, s[10:11]
	v_addc_co_u32_e64 v8, s[20:21], 0, v8, s[8:9]
	s_add_u32 s28, s28, s31
	v_cmp_le_u32_e64 s[12:13], s6, v208
	s_bcnt1_i32_b64 s29, s[14:15]
	v_cmp_le_u32_e64 s[34:35], s6, v209
	s_add_u32 s28, s28, s29
	v_addc_co_u32_e64 v8, s[20:21], 0, v8, s[12:13]
	s_bcnt1_i32_b64 s30, s[34:35]
	v_cmp_le_u32_e64 s[10:11], s6, v210
	s_add_u32 s28, s28, s30
	v_cmp_le_u32_e64 s[16:17], s6, v211
	s_bcnt1_i32_b64 s31, s[10:11]
	v_cmp_le_u32_e64 s[14:15], s6, v212
	s_add_u32 s28, s28, s31
	v_addc_co_u32_e64 v8, s[20:21], 0, v8, s[16:17]
	s_bcnt1_i32_b64 s29, s[14:15]
	v_cmp_le_u32_e64 s[8:9], s6, v213
	s_add_u32 s28, s28, s29
	v_cmp_le_u32_e64 s[34:35], s6, v214
	v_addc_co_u32_e64 v8, s[20:21], 0, v8, s[8:9]
	v_cmp_le_u32_e64 s[10:11], s6, v215
	s_bcnt1_i32_b64 s30, s[34:35]
	v_cmp_le_u32_e64 s[12:13], s6, v216
	s_add_u32 s28, s28, s30
	v_cmp_le_u32_e64 s[14:15], s6, v217
	s_bcnt1_i32_b64 s31, s[10:11]
	v_addc_co_u32_e64 v8, s[20:21], 0, v8, s[12:13]
	s_add_u32 s28, s28, s31
	s_bcnt1_i32_b64 s29, s[14:15]
	s_add_u32 s28, s28, s29
	v_and_b32_e32 v9, 8, v8
	v_cmp_ne_u32_e64 s[18:19], 0, v9
	v_and_b32_e32 v9, 4, v8
	v_cmp_ne_u32_e64 s[16:17], 0, v9
	v_and_b32_e32 v9, 2, v8
	v_cmp_ne_u32_e64 s[12:13], 0, v9
	v_and_b32_e32 v9, 1, v8
	v_cmp_ne_u32_e64 s[8:9], 0, v9
	s_bcnt1_i32_b64 s7, s[18:19]
	s_bcnt1_i32_b64 s3, s[16:17]
	s_lshl1_add_u32 s7, s7, s3
	s_bcnt1_i32_b64 s3, s[12:13]
	s_lshl1_add_u32 s7, s7, s3
	s_bcnt1_i32_b64 s3, s[8:9]
	s_lshl1_add_u32 s7, s7, s3
	s_add_u32 s7, s7, s28
	s_cmpk_lt_u32 s7, 0x100
	s_cselect_b32 s4, s4, s6
	s_cmpk_eq_u32 s7, 0x100
	s_cbranch_scc1 .Ltk0_x28
	s_lshr_b32 s5, s5, 1
	s_cbranch_scc1 .Ltk0_l28
	s_branch .Ltk0_orig
.Ltk0_l24:
	s_or_b32 s6, s4, s5
	v_cmp_le_u32_e64 s[10:11], s6, v172
	v_cmp_le_u32_e64 s[8:9], s6, v179
	v_cmp_le_u32_e64 s[14:15], s6, v181
	s_bcnt1_i32_b64 s28, s[10:11]
	v_cndmask_b32_e64 v8, 0, 1, s[8:9]
	s_bcnt1_i32_b64 s29, s[14:15]
	v_cmp_le_u32_e64 s[12:13], s6, v183
	s_add_u32 s28, s28, s29
	v_cmp_le_u32_e64 s[34:35], s6, v185
	v_addc_co_u32_e64 v8, s[20:21], 0, v8, s[12:13]
	v_cmp_le_u32_e64 s[10:11], s6, v187
	s_bcnt1_i32_b64 s30, s[34:35]
	v_cmp_le_u32_e64 s[16:17], s6, v189
	s_add_u32 s28, s28, s30
	v_cmp_le_u32_e64 s[14:15], s6, v190
	s_bcnt1_i32_b64 s31, s[10:11]
	v_addc_co_u32_e64 v8, s[20:21], 0, v8, s[16:17]
	s_add_u32 s28, s28, s31
	v_cmp_le_u32_e64 s[8:9], s6, v191
	s_bcnt1_i32_b64 s29, s[14:15]
	v_cmp_le_u32_e64 s[34:35], s6, v192
	s_add_u32 s28, s28, s29
	v_addc_co_u32_e64 v8, s[20:21], 0, v8, s[8:9]
	s_bcnt1_i32_b64 s30, s[34:35]
	v_cmp_le_u32_e64 s[10:11], s6, v193
	s_add_u32 s28, s28, s30
	v_cmp_le_u32_e64 s[12:13], s6, v194
	s_bcnt1_i32_b64 s31, s[10:11]
	v_cmp_le_u32_e64 s[14:15], s6, v195
	s_add_u32 s28, s28, s31
	v_addc_co_u32_e64 v8, s[20:21], 0, v8, s[12:13]
	s_bcnt1_i32_b64 s29, s[14:15]
	v_cmp_le_u32_e64 s[16:17], s6, v196
	s_add_u32 s28, s28, s29
	v_cmp_le_u32_e64 s[34:35], s6, v198
	v_addc_co_u32_e64 v8, s[20:21], 0, v8, s[16:17]
	v_cmp_le_u32_e64 s[10:11], s6, v200
	s_bcnt1_i32_b64 s30, s[34:35]
	v_cmp_le_u32_e64 s[8:9], s6, v206
	s_add_u32 s28, s28, s30
	v_cmp_le_u32_e64 s[14:15], s6, v207
	s_bcnt1_i32_b64 s31, s[10:11]
	v_addc_co_u32_e64 v8, s[20:21], 0, v8, s[8:9]
	s_add_u32 s28, s28, s31
	v_cmp_le_u32_e64 s[12:13], s6, v208
	s_bcnt1_i32_b64 s29, s[14:15]
	v_cmp_le_u32_e64 s[34:35], s6, v209
	s_add_u32 s28, s28, s29
	v_addc_co_u32_e64 v8, s[20:21], 0, v8, s[12:13]
	s_bcnt1_i32_b64 s30, s[34:35]
	v_cmp_le_u32_e64 s[10:11], s6, v210
	s_add_u32 s28, s28, s30
	v_cmp_le_u32_e64 s[16:17], s6, v211
	s_bcnt1_i32_b64 s31, s[10:11]
	v_cmp_le_u32_e64 s[14:15], s6, v212
	s_add_u32 s28, s28, s31
	v_addc_co_u32_e64 v8, s[20:21], 0, v8, s[16:17]
	s_bcnt1_i32_b64 s29, s[14:15]
	v_cmp_le_u32_e64 s[8:9], s6, v213
	s_add_u32 s28, s28, s29
	s_nop 0
	v_addc_co_u32_e64 v8, s[20:21], 0, v8, s[8:9]
	v_and_b32_e32 v9, 8, v8
	v_cmp_ne_u32_e64 s[18:19], 0, v9
	v_and_b32_e32 v9, 4, v8
	v_cmp_ne_u32_e64 s[16:17], 0, v9
	v_and_b32_e32 v9, 2, v8
	v_cmp_ne_u32_e64 s[12:13], 0, v9
	v_and_b32_e32 v9, 1, v8
	v_cmp_ne_u32_e64 s[8:9], 0, v9
	s_bcnt1_i32_b64 s7, s[18:19]
	s_bcnt1_i32_b64 s3, s[16:17]
	s_lshl1_add_u32 s7, s7, s3
	s_bcnt1_i32_b64 s3, s[12:13]
	s_lshl1_add_u32 s7, s7, s3
	s_bcnt1_i32_b64 s3, s[8:9]
	s_lshl1_add_u32 s7, s7, s3
	s_add_u32 s7, s7, s28
	s_cmpk_lt_u32 s7, 0x100
	s_cselect_b32 s4, s4, s6
	s_cmpk_eq_u32 s7, 0x100
	s_cbranch_scc1 .Ltk0_x24
	s_lshr_b32 s5, s5, 1
	s_cbranch_scc1 .Ltk0_l24
	s_branch .Ltk0_orig
.Ltk0_l20:
	s_or_b32 s6, s4, s5
	v_cmp_le_u32_e64 s[10:11], s6, v172
	v_cmp_le_u32_e64 s[8:9], s6, v179
	v_cmp_le_u32_e64 s[14:15], s6, v181
	s_bcnt1_i32_b64 s28, s[10:11]
	v_cndmask_b32_e64 v8, 0, 1, s[8:9]
	s_bcnt1_i32_b64 s29, s[14:15]
	v_cmp_le_u32_e64 s[12:13], s6, v183
	s_add_u32 s28, s28, s29
	v_cmp_le_u32_e64 s[34:35], s6, v185
	v_addc_co_u32_e64 v8, s[20:21], 0, v8, s[12:13]
	v_cmp_le_u32_e64 s[10:11], s6, v187
	s_bcnt1_i32_b64 s30, s[34:35]
	v_cmp_le_u32_e64 s[16:17], s6, v189
	s_add_u32 s28, s28, s30
	v_cmp_le_u32_e64 s[14:15], s6, v190
	s_bcnt1_i32_b64 s31, s[10:11]
	v_addc_co_u32_e64 v8, s[20:21], 0, v8, s[16:17]
	s_add_u32 s28, s28, s31
	v_cmp_le_u32_e64 s[8:9], s6, v191
	s_bcnt1_i32_b64 s29, s[14:15]
	v_cmp_le_u32_e64 s[34:35], s6, v192
	s_add_u32 s28, s28, s29
	v_addc_co_u32_e64 v8, s[20:21], 0, v8, s[8:9]
	s_bcnt1_i32_b64 s30, s[34:35]
	v_cmp_le_u32_e64 s[10:11], s6, v193
	s_add_u32 s28, s28, s30
	v_cmp_le_u32_e64 s[12:13], s6, v194
	s_bcnt1_i32_b64 s31, s[10:11]
	v_cmp_le_u32_e64 s[14:15], s6, v195
	s_add_u32 s28, s28, s31
	v_addc_co_u32_e64 v8, s[20:21], 0, v8, s[12:13]
	s_bcnt1_i32_b64 s29, s[14:15]
	v_cmp_le_u32_e64 s[16:17], s6, v196
	s_add_u32 s28, s28, s29
	v_cmp_le_u32_e64 s[34:35], s6, v198
	v_addc_co_u32_e64 v8, s[20:21], 0, v8, s[16:17]
	v_cmp_le_u32_e64 s[10:11], s6, v200
	s_bcnt1_i32_b64 s30, s[34:35]
	v_cmp_le_u32_e64 s[8:9], s6, v206
	s_add_u32 s28, s28, s30
	v_cmp_le_u32_e64 s[14:15], s6, v207
	s_bcnt1_i32_b64 s31, s[10:11]
	v_addc_co_u32_e64 v8, s[20:21], 0, v8, s[8:9]
	s_add_u32 s28, s28, s31
	v_cmp_le_u32_e64 s[12:13], s6, v208
	s_bcnt1_i32_b64 s29, s[14:15]
	v_cmp_le_u32_e64 s[34:35], s6, v209
	s_add_u32 s28, s28, s29
	v_addc_co_u32_e64 v8, s[20:21], 0, v8, s[12:13]
	s_bcnt1_i32_b64 s30, s[34:35]
	s_add_u32 s28, s28, s30
	v_and_b32_e32 v9, 8, v8
	v_cmp_ne_u32_e64 s[18:19], 0, v9
	v_and_b32_e32 v9, 4, v8
	v_cmp_ne_u32_e64 s[16:17], 0, v9
	v_and_b32_e32 v9, 2, v8
	v_cmp_ne_u32_e64 s[12:13], 0, v9
	v_and_b32_e32 v9, 1, v8
	v_cmp_ne_u32_e64 s[8:9], 0, v9
	s_bcnt1_i32_b64 s7, s[18:19]
	s_bcnt1_i32_b64 s3, s[16:17]
	s_lshl1_add_u32 s7, s7, s3
	s_bcnt1_i32_b64 s3, s[12:13]
	s_lshl1_add_u32 s7, s7, s3
	s_bcnt1_i32_b64 s3, s[8:9]
	s_lshl1_add_u32 s7, s7, s3
	s_add_u32 s7, s7, s28
	s_cmpk_lt_u32 s7, 0x100
	s_cselect_b32 s4, s4, s6
	s_cmpk_eq_u32 s7, 0x100
	s_cbranch_scc1 .Ltk0_x20
	s_lshr_b32 s5, s5, 1
	s_cbranch_scc1 .Ltk0_l20
	s_branch .Ltk0_orig
.Ltk0_l16:
	s_or_b32 s6, s4, s5
	v_cmp_le_u32_e64 s[10:11], s6, v172
	v_cmp_le_u32_e64 s[8:9], s6, v179
	v_cmp_le_u32_e64 s[14:15], s6, v181
	s_bcnt1_i32_b64 s28, s[10:11]
	v_cndmask_b32_e64 v8, 0, 1, s[8:9]
	s_bcnt1_i32_b64 s29, s[14:15]
	v_cmp_le_u32_e64 s[12:13], s6, v183
	s_add_u32 s28, s28, s29
	v_cmp_le_u32_e64 s[34:35], s6, v185
	v_addc_co_u32_e64 v8, s[20:21], 0, v8, s[12:13]
	v_cmp_le_u32_e64 s[10:11], s6, v187
	s_bcnt1_i32_b64 s30, s[34:35]
	v_cmp_le_u32_e64 s[16:17], s6, v189
	s_add_u32 s28, s28, s30
	v_cmp_le_u32_e64 s[14:15], s6, v190
	s_bcnt1_i32_b64 s31, s[10:11]
	v_addc_co_u32_e64 v8, s[20:21], 0, v8, s[16:17]
	s_add_u32 s28, s28, s31
	v_cmp_le_u32_e64 s[8:9], s6, v191
	s_bcnt1_i32_b64 s29, s[14:15]
	v_cmp_le_u32_e64 s[34:35], s6, v192
	s_add_u32 s28, s28, s29
	v_addc_co_u32_e64 v8, s[20:21], 0, v8, s[8:9]
	s_bcnt1_i32_b64 s30, s[34:35]
	v_cmp_le_u32_e64 s[10:11], s6, v193
	s_add_u32 s28, s28, s30
	v_cmp_le_u32_e64 s[12:13], s6, v194
	s_bcnt1_i32_b64 s31, s[10:11]
	v_cmp_le_u32_e64 s[14:15], s6, v195
	s_add_u32 s28, s28, s31
	v_addc_co_u32_e64 v8, s[20:21], 0, v8, s[12:13]
	s_bcnt1_i32_b64 s29, s[14:15]
	v_cmp_le_u32_e64 s[16:17], s6, v196
	s_add_u32 s28, s28, s29
	v_cmp_le_u32_e64 s[34:35], s6, v198
	v_addc_co_u32_e64 v8, s[20:21], 0, v8, s[16:17]
	v_cmp_le_u32_e64 s[10:11], s6, v200
	s_bcnt1_i32_b64 s30, s[34:35]
	s_add_u32 s28, s28, s30
	s_bcnt1_i32_b64 s31, s[10:11]
	s_add_u32 s28, s28, s31
	v_and_b32_e32 v9, 4, v8
	v_cmp_ne_u32_e64 s[16:17], 0, v9
	v_and_b32_e32 v9, 2, v8
	v_cmp_ne_u32_e64 s[12:13], 0, v9
	v_and_b32_e32 v9, 1, v8
	v_cmp_ne_u32_e64 s[8:9], 0, v9
	s_bcnt1_i32_b64 s7, s[16:17]
	s_bcnt1_i32_b64 s3, s[12:13]
	s_lshl1_add_u32 s7, s7, s3
	s_bcnt1_i32_b64 s3, s[8:9]
	s_lshl1_add_u32 s7, s7, s3
	s_add_u32 s7, s7, s28
	s_cmpk_lt_u32 s7, 0x100
	s_cselect_b32 s4, s4, s6
	s_cmpk_eq_u32 s7, 0x100
	s_cbranch_scc1 .Ltk0_x16
	s_lshr_b32 s5, s5, 1
	s_cbranch_scc1 .Ltk0_l16
	s_branch .Ltk0_orig
.Ltk0_l12:
	s_or_b32 s6, s4, s5
	v_cmp_le_u32_e64 s[10:11], s6, v172
	v_cmp_le_u32_e64 s[8:9], s6, v179
	v_cmp_le_u32_e64 s[14:15], s6, v181
	s_bcnt1_i32_b64 s28, s[10:11]
	v_cndmask_b32_e64 v8, 0, 1, s[8:9]
	s_bcnt1_i32_b64 s29, s[14:15]
	v_cmp_le_u32_e64 s[12:13], s6, v183
	s_add_u32 s28, s28, s29
	v_cmp_le_u32_e64 s[34:35], s6, v185
	v_addc_co_u32_e64 v8, s[20:21], 0, v8, s[12:13]
	v_cmp_le_u32_e64 s[10:11], s6, v187
	s_bcnt1_i32_b64 s30, s[34:35]
	v_cmp_le_u32_e64 s[16:17], s6, v189
	s_add_u32 s28, s28, s30
	v_cmp_le_u32_e64 s[14:15], s6, v190
	s_bcnt1_i32_b64 s31, s[10:11]
	v_addc_co_u32_e64 v8, s[20:21], 0, v8, s[16:17]
	s_add_u32 s28, s28, s31
	v_cmp_le_u32_e64 s[8:9], s6, v191
	s_bcnt1_i32_b64 s29, s[14:15]
	v_cmp_le_u32_e64 s[34:35], s6, v192
	s_add_u32 s28, s28, s29
	v_addc_co_u32_e64 v8, s[20:21], 0, v8, s[8:9]
	s_bcnt1_i32_b64 s30, s[34:35]
	v_cmp_le_u32_e64 s[10:11], s6, v193
	s_add_u32 s28, s28, s30
	v_cmp_le_u32_e64 s[12:13], s6, v194
	s_bcnt1_i32_b64 s31, s[10:11]
	s_add_u32 s28, s28, s31
	v_addc_co_u32_e64 v8, s[20:21], 0, v8, s[12:13]
	v_and_b32_e32 v9, 4, v8
	v_cmp_ne_u32_e64 s[16:17], 0, v9
	v_and_b32_e32 v9, 2, v8
	v_cmp_ne_u32_e64 s[12:13], 0, v9
	v_and_b32_e32 v9, 1, v8
	v_cmp_ne_u32_e64 s[8:9], 0, v9
	s_bcnt1_i32_b64 s7, s[16:17]
	s_bcnt1_i32_b64 s3, s[12:13]
	s_lshl1_add_u32 s7, s7, s3
	s_bcnt1_i32_b64 s3, s[8:9]
	s_lshl1_add_u32 s7, s7, s3
	s_add_u32 s7, s7, s28
	s_cmpk_lt_u32 s7, 0x100
	s_cselect_b32 s4, s4, s6
	s_cmpk_eq_u32 s7, 0x100
	s_cbranch_scc1 .Ltk0_x12
	s_lshr_b32 s5, s5, 1
	s_cbranch_scc1 .Ltk0_l12
	s_branch .Ltk0_orig
.Ltk0_l8:
	s_or_b32 s6, s4, s5
	v_cmp_le_u32_e64 s[10:11], s6, v172
	v_cmp_le_u32_e64 s[8:9], s6, v179
	v_cmp_le_u32_e64 s[14:15], s6, v181
	s_bcnt1_i32_b64 s28, s[10:11]
	v_cndmask_b32_e64 v8, 0, 1, s[8:9]
	s_bcnt1_i32_b64 s29, s[14:15]
	v_cmp_le_u32_e64 s[12:13], s6, v183
	s_add_u32 s28, s28, s29
	v_cmp_le_u32_e64 s[34:35], s6, v185
	v_addc_co_u32_e64 v8, s[20:21], 0, v8, s[12:13]
	v_cmp_le_u32_e64 s[10:11], s6, v187
	s_bcnt1_i32_b64 s30, s[34:35]
	v_cmp_le_u32_e64 s[16:17], s6, v189
	s_add_u32 s28, s28, s30
	v_cmp_le_u32_e64 s[14:15], s6, v190
	s_bcnt1_i32_b64 s31, s[10:11]
	v_addc_co_u32_e64 v8, s[20:21], 0, v8, s[16:17]
	s_add_u32 s28, s28, s31
	s_bcnt1_i32_b64 s29, s[14:15]
	s_add_u32 s28, s28, s29
	v_and_b32_e32 v9, 2, v8
	v_cmp_ne_u32_e64 s[12:13], 0, v9
	v_and_b32_e32 v9, 1, v8
	v_cmp_ne_u32_e64 s[8:9], 0, v9
	s_bcnt1_i32_b64 s7, s[12:13]
	s_bcnt1_i32_b64 s3, s[8:9]
	s_lshl1_add_u32 s7, s7, s3
	s_add_u32 s7, s7, s28
	s_cmpk_lt_u32 s7, 0x100
	s_cselect_b32 s4, s4, s6
	s_cmpk_eq_u32 s7, 0x100
	s_cbranch_scc1 .Ltk0_x8
	s_lshr_b32 s5, s5, 1
	s_cbranch_scc1 .Ltk0_l8
	s_branch .Ltk0_orig

.Ltk1_l32:
	s_or_b32 s6, s4, s5
	v_cmp_le_u32_e64 s[10:11], s6, v140
	v_cmp_le_u32_e64 s[8:9], s6, v142
	v_cmp_le_u32_e64 s[14:15], s6, v144
	s_bcnt1_i32_b64 s28, s[10:11]
	v_cndmask_b32_e64 v8, 0, 1, s[8:9]
	s_bcnt1_i32_b64 s29, s[14:15]
	v_cmp_le_u32_e64 s[12:13], s6, v146
	s_add_u32 s28, s28, s29
	v_cmp_le_u32_e64 s[34:35], s6, v148
	v_addc_co_u32_e64 v8, s[20:21], 0, v8, s[12:13]
	v_cmp_le_u32_e64 s[10:11], s6, v150
	s_bcnt1_i32_b64 s30, s[34:35]
	v_cmp_le_u32_e64 s[16:17], s6, v152
	s_add_u32 s28, s28, s30
	v_cmp_le_u32_e64 s[14:15], s6, v153
	s_bcnt1_i32_b64 s31, s[10:11]
	v_addc_co_u32_e64 v8, s[20:21], 0, v8, s[16:17]
	s_add_u32 s28, s28, s31
	v_cmp_le_u32_e64 s[8:9], s6, v154
	s_bcnt1_i32_b64 s29, s[14:15]
	v_cmp_le_u32_e64 s[34:35], s6, v155
	s_add_u32 s28, s28, s29
	v_addc_co_u32_e64 v8, s[20:21], 0, v8, s[8:9]
	s_bcnt1_i32_b64 s30, s[34:35]
	v_cmp_le_u32_e64 s[10:11], s6, v156
	s_add_u32 s28, s28, s30
	v_cmp_le_u32_e64 s[12:13], s6, v157
	s_bcnt1_i32_b64 s31, s[10:11]
	v_cmp_le_u32_e64 s[14:15], s6, v158
	s_add_u32 s28, s28, s31
	v_addc_co_u32_e64 v8, s[20:21], 0, v8, s[12:13]
	s_bcnt1_i32_b64 s29, s[14:15]
	v_cmp_le_u32_e64 s[16:17], s6, v159
	s_add_u32 s28, s28, s29
	v_cmp_le_u32_e64 s[34:35], s6, v161
	v_addc_co_u32_e64 v8, s[20:21], 0, v8, s[16:17]
	v_cmp_le_u32_e64 s[10:11], s6, v164
	s_bcnt1_i32_b64 s30, s[34:35]
	v_cmp_le_u32_e64 s[8:9], s6, v170
	s_add_u32 s28, s28, s30
	v_cmp_le_u32_e64 s[14:15], s6, v171
	s_bcnt1_i32_b64 s31, s[10:11]
	v_addc_co_u32_e64 v8, s[20:21], 0, v8, s[8:9]
	s_add_u32 s28, s28, s31
	v_cmp_le_u32_e64 s[12:13], s6, v173
	s_bcnt1_i32_b64 s29, s[14:15]
	v_cmp_le_u32_e64 s[34:35], s6, v180
	s_add_u32 s28, s28, s29
	v_addc_co_u32_e64 v8, s[20:21], 0, v8, s[12:13]
	s_bcnt1_i32_b64 s30, s[34:35]
	v_cmp_le_u32_e64 s[10:11], s6, v182
	s_add_u32 s28, s28, s30
	v_cmp_le_u32_e64 s[16:17], s6, v184
	s_bcnt1_i32_b64 s31, s[10:11]
	v_cmp_le_u32_e64 s[14:15], s6, v186
	s_add_u32 s28, s28, s31
	v_addc_co_u32_e64 v8, s[20:21], 0, v8, s[16:17]
	s_bcnt1_i32_b64 s29, s[14:15]
	v_cmp_le_u32_e64 s[8:9], s6, v188
	s_add_u32 s28, s28, s29
	v_cmp_le_u32_e64 s[34:35], s6, v197
	v_addc_co_u32_e64 v8, s[20:21], 0, v8, s[8:9]
	v_cmp_le_u32_e64 s[10:11], s6, v199
	s_bcnt1_i32_b64 s30, s[34:35]
	v_cmp_le_u32_e64 s[12:13], s6, v201
	s_add_u32 s28, s28, s30
	v_cmp_le_u32_e64 s[14:15], s6, v202
	s_bcnt1_i32_b64 s31, s[10:11]
	v_addc_co_u32_e64 v8, s[20:21], 0, v8, s[12:13]
	s_add_u32 s28, s28, s31
	v_cmp_le_u32_e64 s[16:17], s6, v203
	s_bcnt1_i32_b64 s29, s[14:15]
	v_cmp_le_u32_e64 s[34:35], s6, v204
	s_add_u32 s28, s28, s29
	v_addc_co_u32_e64 v8, s[20:21], 0, v8, s[16:17]
	s_bcnt1_i32_b64 s30, s[34:35]
	v_cmp_le_u32_e64 s[10:11], s6, v205
	s_add_u32 s28, s28, s30
	v_cmp_le_u32_e64 s[8:9], s6, v7
	s_bcnt1_i32_b64 s31, s[10:11]
	s_add_u32 s28, s28, s31
	v_addc_co_u32_e64 v8, s[20:21], 0, v8, s[8:9]
	v_and_b32_e32 v9, 8, v8
	v_cmp_ne_u32_e64 s[18:19], 0, v9
	v_and_b32_e32 v9, 4, v8
	v_cmp_ne_u32_e64 s[16:17], 0, v9
	v_and_b32_e32 v9, 2, v8
	v_cmp_ne_u32_e64 s[12:13], 0, v9
	v_and_b32_e32 v9, 1, v8
	v_cmp_ne_u32_e64 s[8:9], 0, v9
	s_bcnt1_i32_b64 s7, s[18:19]
	s_bcnt1_i32_b64 s3, s[16:17]
	s_lshl1_add_u32 s7, s7, s3
	s_bcnt1_i32_b64 s3, s[12:13]
	s_lshl1_add_u32 s7, s7, s3
	s_bcnt1_i32_b64 s3, s[8:9]
	s_lshl1_add_u32 s7, s7, s3
	s_add_u32 s7, s7, s28
	s_cmpk_lt_u32 s7, 0x100
	s_cselect_b32 s4, s4, s6
	s_cmpk_eq_u32 s7, 0x100
	s_cbranch_scc1 .Ltk1_x32
	s_lshr_b32 s5, s5, 1
	s_cbranch_scc1 .Ltk1_l32
	s_branch .Ltk1_orig
.Ltk1_l28:
	s_or_b32 s6, s4, s5
	v_cmp_le_u32_e64 s[10:11], s6, v140
	v_cmp_le_u32_e64 s[8:9], s6, v142
	v_cmp_le_u32_e64 s[14:15], s6, v144
	s_bcnt1_i32_b64 s28, s[10:11]
	v_cndmask_b32_e64 v8, 0, 1, s[8:9]
	s_bcnt1_i32_b64 s29, s[14:15]
	v_cmp_le_u32_e64 s[12:13], s6, v146
	s_add_u32 s28, s28, s29
	v_cmp_le_u32_e64 s[34:35], s6, v148
	v_addc_co_u32_e64 v8, s[20:21], 0, v8, s[12:13]
	v_cmp_le_u32_e64 s[10:11], s6, v150
	s_bcnt1_i32_b64 s30, s[34:35]
	v_cmp_le_u32_e64 s[16:17], s6, v152
	s_add_u32 s28, s28, s30
	v_cmp_le_u32_e64 s[14:15], s6, v153
	s_bcnt1_i32_b64 s31, s[10:11]
	v_addc_co_u32_e64 v8, s[20:21], 0, v8, s[16:17]
	s_add_u32 s28, s28, s31
	v_cmp_le_u32_e64 s[8:9], s6, v154
	s_bcnt1_i32_b64 s29, s[14:15]
	v_cmp_le_u32_e64 s[34:35], s6, v155
	s_add_u32 s28, s28, s29
	v_addc_co_u32_e64 v8, s[20:21], 0, v8, s[8:9]
	s_bcnt1_i32_b64 s30, s[34:35]
	v_cmp_le_u32_e64 s[10:11], s6, v156
	s_add_u32 s28, s28, s30
	v_cmp_le_u32_e64 s[12:13], s6, v157
	s_bcnt1_i32_b64 s31, s[10:11]
	v_cmp_le_u32_e64 s[14:15], s6, v158
	s_add_u32 s28, s28, s31
	v_addc_co_u32_e64 v8, s[20:21], 0, v8, s[12:13]
	s_bcnt1_i32_b64 s29, s[14:15]
	v_cmp_le_u32_e64 s[16:17], s6, v159
	s_add_u32 s28, s28, s29
	v_cmp_le_u32_e64 s[34:35], s6, v161
	v_addc_co_u32_e64 v8, s[20:21], 0, v8, s[16:17]
	v_cmp_le_u32_e64 s[10:11], s6, v164
	s_bcnt1_i32_b64 s30, s[34:35]
	v_cmp_le_u32_e64 s[8:9], s6, v170
	s_add_u32 s28, s28, s30
	v_cmp_le_u32_e64 s[14:15], s6, v171
	s_bcnt1_i32_b64 s31, s[10:11]
	v_addc_co_u32_e64 v8, s[20:21], 0, v8, s[8:9]
	s_add_u32 s28, s28, s31
	v_cmp_le_u32_e64 s[12:13], s6, v173
	s_bcnt1_i32_b64 s29, s[14:15]
	v_cmp_le_u32_e64 s[34:35], s6, v180
	s_add_u32 s28, s28, s29
	v_addc_co_u32_e64 v8, s[20:21], 0, v8, s[12:13]
	s_bcnt1_i32_b64 s30, s[34:35]
	v_cmp_le_u32_e64 s[10:11], s6, v182
	s_add_u32 s28, s28, s30
	v_cmp_le_u32_e64 s[16:17], s6, v184
	s_bcnt1_i32_b64 s31, s[10:11]
	v_cmp_le_u32_e64 s[14:15], s6, v186
	s_add_u32 s28, s28, s31
	v_addc_co_u32_e64 v8, s[20:21], 0, v8, s[16:17]
	s_bcnt1_i32_b64 s29, s[14:15]
	v_cmp_le_u32_e64 s[8:9], s6, v188
	s_add_u32 s28, s28, s29
	v_cmp_le_u32_e64 s[34:35], s6, v197
	v_addc_co_u32_e64 v8, s[20:21], 0, v8, s[8:9]
	v_cmp_le_u32_e64 s[10:11], s6, v199
	s_bcnt1_i32_b64 s30, s[34:35]
	v_cmp_le_u32_e64 s[12:13], s6, v201
	s_add_u32 s28, s28, s30
	v_cmp_le_u32_e64 s[14:15], s6, v202
	s_bcnt1_i32_b64 s31, s[10:11]
	v_addc_co_u32_e64 v8, s[20:21], 0, v8, s[12:13]
	s_add_u32 s28, s28, s31
	s_bcnt1_i32_b64 s29, s[14:15]
	s_add_u32 s28, s28, s29
	v_and_b32_e32 v9, 8, v8
	v_cmp_ne_u32_e64 s[18:19], 0, v9
	v_and_b32_e32 v9, 4, v8
	v_cmp_ne_u32_e64 s[16:17], 0, v9
	v_and_b32_e32 v9, 2, v8
	v_cmp_ne_u32_e64 s[12:13], 0, v9
	v_and_b32_e32 v9, 1, v8
	v_cmp_ne_u32_e64 s[8:9], 0, v9
	s_bcnt1_i32_b64 s7, s[18:19]
	s_bcnt1_i32_b64 s3, s[16:17]
	s_lshl1_add_u32 s7, s7, s3
	s_bcnt1_i32_b64 s3, s[12:13]
	s_lshl1_add_u32 s7, s7, s3
	s_bcnt1_i32_b64 s3, s[8:9]
	s_lshl1_add_u32 s7, s7, s3
	s_add_u32 s7, s7, s28
	s_cmpk_lt_u32 s7, 0x100
	s_cselect_b32 s4, s4, s6
	s_cmpk_eq_u32 s7, 0x100
	s_cbranch_scc1 .Ltk1_x28
	s_lshr_b32 s5, s5, 1
	s_cbranch_scc1 .Ltk1_l28
	s_branch .Ltk1_orig
.Ltk1_l24:
	s_or_b32 s6, s4, s5
	v_cmp_le_u32_e64 s[10:11], s6, v140
	v_cmp_le_u32_e64 s[8:9], s6, v142
	v_cmp_le_u32_e64 s[14:15], s6, v144
	s_bcnt1_i32_b64 s28, s[10:11]
	v_cndmask_b32_e64 v8, 0, 1, s[8:9]
	s_bcnt1_i32_b64 s29, s[14:15]
	v_cmp_le_u32_e64 s[12:13], s6, v146
	s_add_u32 s28, s28, s29
	v_cmp_le_u32_e64 s[34:35], s6, v148
	v_addc_co_u32_e64 v8, s[20:21], 0, v8, s[12:13]
	v_cmp_le_u32_e64 s[10:11], s6, v150
	s_bcnt1_i32_b64 s30, s[34:35]
	v_cmp_le_u32_e64 s[16:17], s6, v152
	s_add_u32 s28, s28, s30
	v_cmp_le_u32_e64 s[14:15], s6, v153
	s_bcnt1_i32_b64 s31, s[10:11]
	v_addc_co_u32_e64 v8, s[20:21], 0, v8, s[16:17]
	s_add_u32 s28, s28, s31
	v_cmp_le_u32_e64 s[8:9], s6, v154
	s_bcnt1_i32_b64 s29, s[14:15]
	v_cmp_le_u32_e64 s[34:35], s6, v155
	s_add_u32 s28, s28, s29
	v_addc_co_u32_e64 v8, s[20:21], 0, v8, s[8:9]
	s_bcnt1_i32_b64 s30, s[34:35]
	v_cmp_le_u32_e64 s[10:11], s6, v156
	s_add_u32 s28, s28, s30
	v_cmp_le_u32_e64 s[12:13], s6, v157
	s_bcnt1_i32_b64 s31, s[10:11]
	v_cmp_le_u32_e64 s[14:15], s6, v158
	s_add_u32 s28, s28, s31
	v_addc_co_u32_e64 v8, s[20:21], 0, v8, s[12:13]
	s_bcnt1_i32_b64 s29, s[14:15]
	v_cmp_le_u32_e64 s[16:17], s6, v159
	s_add_u32 s28, s28, s29
	v_cmp_le_u32_e64 s[34:35], s6, v161
	v_addc_co_u32_e64 v8, s[20:21], 0, v8, s[16:17]
	v_cmp_le_u32_e64 s[10:11], s6, v164
	s_bcnt1_i32_b64 s30, s[34:35]
	v_cmp_le_u32_e64 s[8:9], s6, v170
	s_add_u32 s28, s28, s30
	v_cmp_le_u32_e64 s[14:15], s6, v171
	s_bcnt1_i32_b64 s31, s[10:11]
	v_addc_co_u32_e64 v8, s[20:21], 0, v8, s[8:9]
	s_add_u32 s28, s28, s31
	v_cmp_le_u32_e64 s[12:13], s6, v173
	s_bcnt1_i32_b64 s29, s[14:15]
	v_cmp_le_u32_e64 s[34:35], s6, v180
	s_add_u32 s28, s28, s29
	v_addc_co_u32_e64 v8, s[20:21], 0, v8, s[12:13]
	s_bcnt1_i32_b64 s30, s[34:35]
	v_cmp_le_u32_e64 s[10:11], s6, v182
	s_add_u32 s28, s28, s30
	v_cmp_le_u32_e64 s[16:17], s6, v184
	s_bcnt1_i32_b64 s31, s[10:11]
	v_cmp_le_u32_e64 s[14:15], s6, v186
	s_add_u32 s28, s28, s31
	v_addc_co_u32_e64 v8, s[20:21], 0, v8, s[16:17]
	s_bcnt1_i32_b64 s29, s[14:15]
	v_cmp_le_u32_e64 s[8:9], s6, v188
	s_add_u32 s28, s28, s29
	s_nop 0
	v_addc_co_u32_e64 v8, s[20:21], 0, v8, s[8:9]
	v_and_b32_e32 v9, 8, v8
	v_cmp_ne_u32_e64 s[18:19], 0, v9
	v_and_b32_e32 v9, 4, v8
	v_cmp_ne_u32_e64 s[16:17], 0, v9
	v_and_b32_e32 v9, 2, v8
	v_cmp_ne_u32_e64 s[12:13], 0, v9
	v_and_b32_e32 v9, 1, v8
	v_cmp_ne_u32_e64 s[8:9], 0, v9
	s_bcnt1_i32_b64 s7, s[18:19]
	s_bcnt1_i32_b64 s3, s[16:17]
	s_lshl1_add_u32 s7, s7, s3
	s_bcnt1_i32_b64 s3, s[12:13]
	s_lshl1_add_u32 s7, s7, s3
	s_bcnt1_i32_b64 s3, s[8:9]
	s_lshl1_add_u32 s7, s7, s3
	s_add_u32 s7, s7, s28
	s_cmpk_lt_u32 s7, 0x100
	s_cselect_b32 s4, s4, s6
	s_cmpk_eq_u32 s7, 0x100
	s_cbranch_scc1 .Ltk1_x24
	s_lshr_b32 s5, s5, 1
	s_cbranch_scc1 .Ltk1_l24
	s_branch .Ltk1_orig
.Ltk1_l20:
	s_or_b32 s6, s4, s5
	v_cmp_le_u32_e64 s[10:11], s6, v140
	v_cmp_le_u32_e64 s[8:9], s6, v142
	v_cmp_le_u32_e64 s[14:15], s6, v144
	s_bcnt1_i32_b64 s28, s[10:11]
	v_cndmask_b32_e64 v8, 0, 1, s[8:9]
	s_bcnt1_i32_b64 s29, s[14:15]
	v_cmp_le_u32_e64 s[12:13], s6, v146
	s_add_u32 s28, s28, s29
	v_cmp_le_u32_e64 s[34:35], s6, v148
	v_addc_co_u32_e64 v8, s[20:21], 0, v8, s[12:13]
	v_cmp_le_u32_e64 s[10:11], s6, v150
	s_bcnt1_i32_b64 s30, s[34:35]
	v_cmp_le_u32_e64 s[16:17], s6, v152
	s_add_u32 s28, s28, s30
	v_cmp_le_u32_e64 s[14:15], s6, v153
	s_bcnt1_i32_b64 s31, s[10:11]
	v_addc_co_u32_e64 v8, s[20:21], 0, v8, s[16:17]
	s_add_u32 s28, s28, s31
	v_cmp_le_u32_e64 s[8:9], s6, v154
	s_bcnt1_i32_b64 s29, s[14:15]
	v_cmp_le_u32_e64 s[34:35], s6, v155
	s_add_u32 s28, s28, s29
	v_addc_co_u32_e64 v8, s[20:21], 0, v8, s[8:9]
	s_bcnt1_i32_b64 s30, s[34:35]
	v_cmp_le_u32_e64 s[10:11], s6, v156
	s_add_u32 s28, s28, s30
	v_cmp_le_u32_e64 s[12:13], s6, v157
	s_bcnt1_i32_b64 s31, s[10:11]
	v_cmp_le_u32_e64 s[14:15], s6, v158
	s_add_u32 s28, s28, s31
	v_addc_co_u32_e64 v8, s[20:21], 0, v8, s[12:13]
	s_bcnt1_i32_b64 s29, s[14:15]
	v_cmp_le_u32_e64 s[16:17], s6, v159
	s_add_u32 s28, s28, s29
	v_cmp_le_u32_e64 s[34:35], s6, v161
	v_addc_co_u32_e64 v8, s[20:21], 0, v8, s[16:17]
	v_cmp_le_u32_e64 s[10:11], s6, v164
	s_bcnt1_i32_b64 s30, s[34:35]
	v_cmp_le_u32_e64 s[8:9], s6, v170
	s_add_u32 s28, s28, s30
	v_cmp_le_u32_e64 s[14:15], s6, v171
	s_bcnt1_i32_b64 s31, s[10:11]
	v_addc_co_u32_e64 v8, s[20:21], 0, v8, s[8:9]
	s_add_u32 s28, s28, s31
	v_cmp_le_u32_e64 s[12:13], s6, v173
	s_bcnt1_i32_b64 s29, s[14:15]
	v_cmp_le_u32_e64 s[34:35], s6, v180
	s_add_u32 s28, s28, s29
	v_addc_co_u32_e64 v8, s[20:21], 0, v8, s[12:13]
	s_bcnt1_i32_b64 s30, s[34:35]
	s_add_u32 s28, s28, s30
	v_and_b32_e32 v9, 8, v8
	v_cmp_ne_u32_e64 s[18:19], 0, v9
	v_and_b32_e32 v9, 4, v8
	v_cmp_ne_u32_e64 s[16:17], 0, v9
	v_and_b32_e32 v9, 2, v8
	v_cmp_ne_u32_e64 s[12:13], 0, v9
	v_and_b32_e32 v9, 1, v8
	v_cmp_ne_u32_e64 s[8:9], 0, v9
	s_bcnt1_i32_b64 s7, s[18:19]
	s_bcnt1_i32_b64 s3, s[16:17]
	s_lshl1_add_u32 s7, s7, s3
	s_bcnt1_i32_b64 s3, s[12:13]
	s_lshl1_add_u32 s7, s7, s3
	s_bcnt1_i32_b64 s3, s[8:9]
	s_lshl1_add_u32 s7, s7, s3
	s_add_u32 s7, s7, s28
	s_cmpk_lt_u32 s7, 0x100
	s_cselect_b32 s4, s4, s6
	s_cmpk_eq_u32 s7, 0x100
	s_cbranch_scc1 .Ltk1_x20
	s_lshr_b32 s5, s5, 1
	s_cbranch_scc1 .Ltk1_l20
	s_branch .Ltk1_orig
.Ltk1_l16:
	s_or_b32 s6, s4, s5
	v_cmp_le_u32_e64 s[10:11], s6, v140
	v_cmp_le_u32_e64 s[8:9], s6, v142
	v_cmp_le_u32_e64 s[14:15], s6, v144
	s_bcnt1_i32_b64 s28, s[10:11]
	v_cndmask_b32_e64 v8, 0, 1, s[8:9]
	s_bcnt1_i32_b64 s29, s[14:15]
	v_cmp_le_u32_e64 s[12:13], s6, v146
	s_add_u32 s28, s28, s29
	v_cmp_le_u32_e64 s[34:35], s6, v148
	v_addc_co_u32_e64 v8, s[20:21], 0, v8, s[12:13]
	v_cmp_le_u32_e64 s[10:11], s6, v150
	s_bcnt1_i32_b64 s30, s[34:35]
	v_cmp_le_u32_e64 s[16:17], s6, v152
	s_add_u32 s28, s28, s30
	v_cmp_le_u32_e64 s[14:15], s6, v153
	s_bcnt1_i32_b64 s31, s[10:11]
	v_addc_co_u32_e64 v8, s[20:21], 0, v8, s[16:17]
	s_add_u32 s28, s28, s31
	v_cmp_le_u32_e64 s[8:9], s6, v154
	s_bcnt1_i32_b64 s29, s[14:15]
	v_cmp_le_u32_e64 s[34:35], s6, v155
	s_add_u32 s28, s28, s29
	v_addc_co_u32_e64 v8, s[20:21], 0, v8, s[8:9]
	s_bcnt1_i32_b64 s30, s[34:35]
	v_cmp_le_u32_e64 s[10:11], s6, v156
	s_add_u32 s28, s28, s30
	v_cmp_le_u32_e64 s[12:13], s6, v157
	s_bcnt1_i32_b64 s31, s[10:11]
	v_cmp_le_u32_e64 s[14:15], s6, v158
	s_add_u32 s28, s28, s31
	v_addc_co_u32_e64 v8, s[20:21], 0, v8, s[12:13]
	s_bcnt1_i32_b64 s29, s[14:15]
	v_cmp_le_u32_e64 s[16:17], s6, v159
	s_add_u32 s28, s28, s29
	v_cmp_le_u32_e64 s[34:35], s6, v161
	v_addc_co_u32_e64 v8, s[20:21], 0, v8, s[16:17]
	v_cmp_le_u32_e64 s[10:11], s6, v164
	s_bcnt1_i32_b64 s30, s[34:35]
	s_add_u32 s28, s28, s30
	s_bcnt1_i32_b64 s31, s[10:11]
	s_add_u32 s28, s28, s31
	v_and_b32_e32 v9, 4, v8
	v_cmp_ne_u32_e64 s[16:17], 0, v9
	v_and_b32_e32 v9, 2, v8
	v_cmp_ne_u32_e64 s[12:13], 0, v9
	v_and_b32_e32 v9, 1, v8
	v_cmp_ne_u32_e64 s[8:9], 0, v9
	s_bcnt1_i32_b64 s7, s[16:17]
	s_bcnt1_i32_b64 s3, s[12:13]
	s_lshl1_add_u32 s7, s7, s3
	s_bcnt1_i32_b64 s3, s[8:9]
	s_lshl1_add_u32 s7, s7, s3
	s_add_u32 s7, s7, s28
	s_cmpk_lt_u32 s7, 0x100
	s_cselect_b32 s4, s4, s6
	s_cmpk_eq_u32 s7, 0x100
	s_cbranch_scc1 .Ltk1_x16
	s_lshr_b32 s5, s5, 1
	s_cbranch_scc1 .Ltk1_l16
	s_branch .Ltk1_orig
.Ltk1_l12:
	s_or_b32 s6, s4, s5
	v_cmp_le_u32_e64 s[10:11], s6, v140
	v_cmp_le_u32_e64 s[8:9], s6, v142
	v_cmp_le_u32_e64 s[14:15], s6, v144
	s_bcnt1_i32_b64 s28, s[10:11]
	v_cndmask_b32_e64 v8, 0, 1, s[8:9]
	s_bcnt1_i32_b64 s29, s[14:15]
	v_cmp_le_u32_e64 s[12:13], s6, v146
	s_add_u32 s28, s28, s29
	v_cmp_le_u32_e64 s[34:35], s6, v148
	v_addc_co_u32_e64 v8, s[20:21], 0, v8, s[12:13]
	v_cmp_le_u32_e64 s[10:11], s6, v150
	s_bcnt1_i32_b64 s30, s[34:35]
	v_cmp_le_u32_e64 s[16:17], s6, v152
	s_add_u32 s28, s28, s30
	v_cmp_le_u32_e64 s[14:15], s6, v153
	s_bcnt1_i32_b64 s31, s[10:11]
	v_addc_co_u32_e64 v8, s[20:21], 0, v8, s[16:17]
	s_add_u32 s28, s28, s31
	v_cmp_le_u32_e64 s[8:9], s6, v154
	s_bcnt1_i32_b64 s29, s[14:15]
	v_cmp_le_u32_e64 s[34:35], s6, v155
	s_add_u32 s28, s28, s29
	v_addc_co_u32_e64 v8, s[20:21], 0, v8, s[8:9]
	s_bcnt1_i32_b64 s30, s[34:35]
	v_cmp_le_u32_e64 s[10:11], s6, v156
	s_add_u32 s28, s28, s30
	v_cmp_le_u32_e64 s[12:13], s6, v157
	s_bcnt1_i32_b64 s31, s[10:11]
	s_add_u32 s28, s28, s31
	v_addc_co_u32_e64 v8, s[20:21], 0, v8, s[12:13]
	v_and_b32_e32 v9, 4, v8
	v_cmp_ne_u32_e64 s[16:17], 0, v9
	v_and_b32_e32 v9, 2, v8
	v_cmp_ne_u32_e64 s[12:13], 0, v9
	v_and_b32_e32 v9, 1, v8
	v_cmp_ne_u32_e64 s[8:9], 0, v9
	s_bcnt1_i32_b64 s7, s[16:17]
	s_bcnt1_i32_b64 s3, s[12:13]
	s_lshl1_add_u32 s7, s7, s3
	s_bcnt1_i32_b64 s3, s[8:9]
	s_lshl1_add_u32 s7, s7, s3
	s_add_u32 s7, s7, s28
	s_cmpk_lt_u32 s7, 0x100
	s_cselect_b32 s4, s4, s6
	s_cmpk_eq_u32 s7, 0x100
	s_cbranch_scc1 .Ltk1_x12
	s_lshr_b32 s5, s5, 1
	s_cbranch_scc1 .Ltk1_l12
	s_branch .Ltk1_orig
.Ltk1_l8:
	s_or_b32 s6, s4, s5
	v_cmp_le_u32_e64 s[10:11], s6, v140
	v_cmp_le_u32_e64 s[8:9], s6, v142
	v_cmp_le_u32_e64 s[14:15], s6, v144
	s_bcnt1_i32_b64 s28, s[10:11]
	v_cndmask_b32_e64 v8, 0, 1, s[8:9]
	s_bcnt1_i32_b64 s29, s[14:15]
	v_cmp_le_u32_e64 s[12:13], s6, v146
	s_add_u32 s28, s28, s29
	v_cmp_le_u32_e64 s[34:35], s6, v148
	v_addc_co_u32_e64 v8, s[20:21], 0, v8, s[12:13]
	v_cmp_le_u32_e64 s[10:11], s6, v150
	s_bcnt1_i32_b64 s30, s[34:35]
	v_cmp_le_u32_e64 s[16:17], s6, v152
	s_add_u32 s28, s28, s30
	v_cmp_le_u32_e64 s[14:15], s6, v153
	s_bcnt1_i32_b64 s31, s[10:11]
	v_addc_co_u32_e64 v8, s[20:21], 0, v8, s[16:17]
	s_add_u32 s28, s28, s31
	s_bcnt1_i32_b64 s29, s[14:15]
	s_add_u32 s28, s28, s29
	v_and_b32_e32 v9, 2, v8
	v_cmp_ne_u32_e64 s[12:13], 0, v9
	v_and_b32_e32 v9, 1, v8
	v_cmp_ne_u32_e64 s[8:9], 0, v9
	s_bcnt1_i32_b64 s7, s[12:13]
	s_bcnt1_i32_b64 s3, s[8:9]
	s_lshl1_add_u32 s7, s7, s3
	s_add_u32 s7, s7, s28
	s_cmpk_lt_u32 s7, 0x100
	s_cselect_b32 s4, s4, s6
	s_cmpk_eq_u32 s7, 0x100
	s_cbranch_scc1 .Ltk1_x8
	s_lshr_b32 s5, s5, 1
	s_cbranch_scc1 .Ltk1_l8
	s_branch .Ltk1_orig

.Ltk2_l32:
	s_or_b32 s6, s4, s5
	v_cmp_le_u32_e64 s[10:11], s6, v111
	v_cmp_le_u32_e64 s[8:9], s6, v113
	v_cmp_le_u32_e64 s[14:15], s6, v115
	s_bcnt1_i32_b64 s28, s[10:11]
	v_cndmask_b32_e64 v8, 0, 1, s[8:9]
	s_bcnt1_i32_b64 s29, s[14:15]
	v_cmp_le_u32_e64 s[12:13], s6, v117
	s_add_u32 s28, s28, s29
	v_cmp_le_u32_e64 s[34:35], s6, v119
	v_addc_co_u32_e64 v8, s[20:21], 0, v8, s[12:13]
	v_cmp_le_u32_e64 s[10:11], s6, v121
	s_bcnt1_i32_b64 s30, s[34:35]
	v_cmp_le_u32_e64 s[16:17], s6, v123
	s_add_u32 s28, s28, s30
	v_cmp_le_u32_e64 s[14:15], s6, v124
	s_bcnt1_i32_b64 s31, s[10:11]
	v_addc_co_u32_e64 v8, s[20:21], 0, v8, s[16:17]
	s_add_u32 s28, s28, s31
	v_cmp_le_u32_e64 s[8:9], s6, v125
	s_bcnt1_i32_b64 s29, s[14:15]
	v_cmp_le_u32_e64 s[34:35], s6, v126
	s_add_u32 s28, s28, s29
	v_addc_co_u32_e64 v8, s[20:21], 0, v8, s[8:9]
	s_bcnt1_i32_b64 s30, s[34:35]
	v_cmp_le_u32_e64 s[10:11], s6, v127
	s_add_u32 s28, s28, s30
	v_cmp_le_u32_e64 s[12:13], s6, v128
	s_bcnt1_i32_b64 s31, s[10:11]
	v_cmp_le_u32_e64 s[14:15], s6, v129
	s_add_u32 s28, s28, s31
	v_addc_co_u32_e64 v8, s[20:21], 0, v8, s[12:13]
	s_bcnt1_i32_b64 s29, s[14:15]
	v_cmp_le_u32_e64 s[16:17], s6, v130
	s_add_u32 s28, s28, s29
	v_cmp_le_u32_e64 s[34:35], s6, v132
	v_addc_co_u32_e64 v8, s[20:21], 0, v8, s[16:17]
	v_cmp_le_u32_e64 s[10:11], s6, v133
	s_bcnt1_i32_b64 s30, s[34:35]
	v_cmp_le_u32_e64 s[8:9], s6, v138
	s_add_u32 s28, s28, s30
	v_cmp_le_u32_e64 s[14:15], s6, v139
	s_bcnt1_i32_b64 s31, s[10:11]
	v_addc_co_u32_e64 v8, s[20:21], 0, v8, s[8:9]
	s_add_u32 s28, s28, s31
	v_cmp_le_u32_e64 s[12:13], s6, v141
	s_bcnt1_i32_b64 s29, s[14:15]
	v_cmp_le_u32_e64 s[34:35], s6, v143
	s_add_u32 s28, s28, s29
	v_addc_co_u32_e64 v8, s[20:21], 0, v8, s[12:13]
	s_bcnt1_i32_b64 s30, s[34:35]
	v_cmp_le_u32_e64 s[10:11], s6, v145
	s_add_u32 s28, s28, s30
	v_cmp_le_u32_e64 s[16:17], s6, v147
	s_bcnt1_i32_b64 s31, s[10:11]
	v_cmp_le_u32_e64 s[14:15], s6, v149
	s_add_u32 s28, s28, s31
	v_addc_co_u32_e64 v8, s[20:21], 0, v8, s[16:17]
	s_bcnt1_i32_b64 s29, s[14:15]
	v_cmp_le_u32_e64 s[8:9], s6, v151
	s_add_u32 s28, s28, s29
	v_cmp_le_u32_e64 s[34:35], s6, v160
	v_addc_co_u32_e64 v8, s[20:21], 0, v8, s[8:9]
	v_cmp_le_u32_e64 s[10:11], s6, v163
	s_bcnt1_i32_b64 s30, s[34:35]
	v_cmp_le_u32_e64 s[12:13], s6, v165
	s_add_u32 s28, s28, s30
	v_cmp_le_u32_e64 s[14:15], s6, v166
	s_bcnt1_i32_b64 s31, s[10:11]
	v_addc_co_u32_e64 v8, s[20:21], 0, v8, s[12:13]
	s_add_u32 s28, s28, s31
	v_cmp_le_u32_e64 s[16:17], s6, v167
	s_bcnt1_i32_b64 s29, s[14:15]
	v_cmp_le_u32_e64 s[34:35], s6, v168
	s_add_u32 s28, s28, s29
	v_addc_co_u32_e64 v8, s[20:21], 0, v8, s[16:17]
	s_bcnt1_i32_b64 s30, s[34:35]
	v_cmp_le_u32_e64 s[10:11], s6, v169
	s_add_u32 s28, s28, s30
	v_cmp_le_u32_e64 s[8:9], s6, v6
	s_bcnt1_i32_b64 s31, s[10:11]
	s_add_u32 s28, s28, s31
	v_addc_co_u32_e64 v8, s[20:21], 0, v8, s[8:9]
	v_and_b32_e32 v9, 8, v8
	v_cmp_ne_u32_e64 s[18:19], 0, v9
	v_and_b32_e32 v9, 4, v8
	v_cmp_ne_u32_e64 s[16:17], 0, v9
	v_and_b32_e32 v9, 2, v8
	v_cmp_ne_u32_e64 s[12:13], 0, v9
	v_and_b32_e32 v9, 1, v8
	v_cmp_ne_u32_e64 s[8:9], 0, v9
	s_bcnt1_i32_b64 s7, s[18:19]
	s_bcnt1_i32_b64 s3, s[16:17]
	s_lshl1_add_u32 s7, s7, s3
	s_bcnt1_i32_b64 s3, s[12:13]
	s_lshl1_add_u32 s7, s7, s3
	s_bcnt1_i32_b64 s3, s[8:9]
	s_lshl1_add_u32 s7, s7, s3
	s_add_u32 s7, s7, s28
	s_cmpk_lt_u32 s7, 0x100
	s_cselect_b32 s4, s4, s6
	s_cmpk_eq_u32 s7, 0x100
	s_cbranch_scc1 .Ltk2_x32
	s_lshr_b32 s5, s5, 1
	s_cbranch_scc1 .Ltk2_l32
	s_branch .Ltk2_orig
.Ltk2_l28:
	s_or_b32 s6, s4, s5
	v_cmp_le_u32_e64 s[10:11], s6, v111
	v_cmp_le_u32_e64 s[8:9], s6, v113
	v_cmp_le_u32_e64 s[14:15], s6, v115
	s_bcnt1_i32_b64 s28, s[10:11]
	v_cndmask_b32_e64 v8, 0, 1, s[8:9]
	s_bcnt1_i32_b64 s29, s[14:15]
	v_cmp_le_u32_e64 s[12:13], s6, v117
	s_add_u32 s28, s28, s29
	v_cmp_le_u32_e64 s[34:35], s6, v119
	v_addc_co_u32_e64 v8, s[20:21], 0, v8, s[12:13]
	v_cmp_le_u32_e64 s[10:11], s6, v121
	s_bcnt1_i32_b64 s30, s[34:35]
	v_cmp_le_u32_e64 s[16:17], s6, v123
	s_add_u32 s28, s28, s30
	v_cmp_le_u32_e64 s[14:15], s6, v124
	s_bcnt1_i32_b64 s31, s[10:11]
	v_addc_co_u32_e64 v8, s[20:21], 0, v8, s[16:17]
	s_add_u32 s28, s28, s31
	v_cmp_le_u32_e64 s[8:9], s6, v125
	s_bcnt1_i32_b64 s29, s[14:15]
	v_cmp_le_u32_e64 s[34:35], s6, v126
	s_add_u32 s28, s28, s29
	v_addc_co_u32_e64 v8, s[20:21], 0, v8, s[8:9]
	s_bcnt1_i32_b64 s30, s[34:35]
	v_cmp_le_u32_e64 s[10:11], s6, v127
	s_add_u32 s28, s28, s30
	v_cmp_le_u32_e64 s[12:13], s6, v128
	s_bcnt1_i32_b64 s31, s[10:11]
	v_cmp_le_u32_e64 s[14:15], s6, v129
	s_add_u32 s28, s28, s31
	v_addc_co_u32_e64 v8, s[20:21], 0, v8, s[12:13]
	s_bcnt1_i32_b64 s29, s[14:15]
	v_cmp_le_u32_e64 s[16:17], s6, v130
	s_add_u32 s28, s28, s29
	v_cmp_le_u32_e64 s[34:35], s6, v132
	v_addc_co_u32_e64 v8, s[20:21], 0, v8, s[16:17]
	v_cmp_le_u32_e64 s[10:11], s6, v133
	s_bcnt1_i32_b64 s30, s[34:35]
	v_cmp_le_u32_e64 s[8:9], s6, v138
	s_add_u32 s28, s28, s30
	v_cmp_le_u32_e64 s[14:15], s6, v139
	s_bcnt1_i32_b64 s31, s[10:11]
	v_addc_co_u32_e64 v8, s[20:21], 0, v8, s[8:9]
	s_add_u32 s28, s28, s31
	v_cmp_le_u32_e64 s[12:13], s6, v141
	s_bcnt1_i32_b64 s29, s[14:15]
	v_cmp_le_u32_e64 s[34:35], s6, v143
	s_add_u32 s28, s28, s29
	v_addc_co_u32_e64 v8, s[20:21], 0, v8, s[12:13]
	s_bcnt1_i32_b64 s30, s[34:35]
	v_cmp_le_u32_e64 s[10:11], s6, v145
	s_add_u32 s28, s28, s30
	v_cmp_le_u32_e64 s[16:17], s6, v147
	s_bcnt1_i32_b64 s31, s[10:11]
	v_cmp_le_u32_e64 s[14:15], s6, v149
	s_add_u32 s28, s28, s31
	v_addc_co_u32_e64 v8, s[20:21], 0, v8, s[16:17]
	s_bcnt1_i32_b64 s29, s[14:15]
	v_cmp_le_u32_e64 s[8:9], s6, v151
	s_add_u32 s28, s28, s29
	v_cmp_le_u32_e64 s[34:35], s6, v160
	v_addc_co_u32_e64 v8, s[20:21], 0, v8, s[8:9]
	v_cmp_le_u32_e64 s[10:11], s6, v163
	s_bcnt1_i32_b64 s30, s[34:35]
	v_cmp_le_u32_e64 s[12:13], s6, v165
	s_add_u32 s28, s28, s30
	v_cmp_le_u32_e64 s[14:15], s6, v166
	s_bcnt1_i32_b64 s31, s[10:11]
	v_addc_co_u32_e64 v8, s[20:21], 0, v8, s[12:13]
	s_add_u32 s28, s28, s31
	s_bcnt1_i32_b64 s29, s[14:15]
	s_add_u32 s28, s28, s29
	v_and_b32_e32 v9, 8, v8
	v_cmp_ne_u32_e64 s[18:19], 0, v9
	v_and_b32_e32 v9, 4, v8
	v_cmp_ne_u32_e64 s[16:17], 0, v9
	v_and_b32_e32 v9, 2, v8
	v_cmp_ne_u32_e64 s[12:13], 0, v9
	v_and_b32_e32 v9, 1, v8
	v_cmp_ne_u32_e64 s[8:9], 0, v9
	s_bcnt1_i32_b64 s7, s[18:19]
	s_bcnt1_i32_b64 s3, s[16:17]
	s_lshl1_add_u32 s7, s7, s3
	s_bcnt1_i32_b64 s3, s[12:13]
	s_lshl1_add_u32 s7, s7, s3
	s_bcnt1_i32_b64 s3, s[8:9]
	s_lshl1_add_u32 s7, s7, s3
	s_add_u32 s7, s7, s28
	s_cmpk_lt_u32 s7, 0x100
	s_cselect_b32 s4, s4, s6
	s_cmpk_eq_u32 s7, 0x100
	s_cbranch_scc1 .Ltk2_x28
	s_lshr_b32 s5, s5, 1
	s_cbranch_scc1 .Ltk2_l28
	s_branch .Ltk2_orig
.Ltk2_l24:
	s_or_b32 s6, s4, s5
	v_cmp_le_u32_e64 s[10:11], s6, v111
	v_cmp_le_u32_e64 s[8:9], s6, v113
	v_cmp_le_u32_e64 s[14:15], s6, v115
	s_bcnt1_i32_b64 s28, s[10:11]
	v_cndmask_b32_e64 v8, 0, 1, s[8:9]
	s_bcnt1_i32_b64 s29, s[14:15]
	v_cmp_le_u32_e64 s[12:13], s6, v117
	s_add_u32 s28, s28, s29
	v_cmp_le_u32_e64 s[34:35], s6, v119
	v_addc_co_u32_e64 v8, s[20:21], 0, v8, s[12:13]
	v_cmp_le_u32_e64 s[10:11], s6, v121
	s_bcnt1_i32_b64 s30, s[34:35]
	v_cmp_le_u32_e64 s[16:17], s6, v123
	s_add_u32 s28, s28, s30
	v_cmp_le_u32_e64 s[14:15], s6, v124
	s_bcnt1_i32_b64 s31, s[10:11]
	v_addc_co_u32_e64 v8, s[20:21], 0, v8, s[16:17]
	s_add_u32 s28, s28, s31
	v_cmp_le_u32_e64 s[8:9], s6, v125
	s_bcnt1_i32_b64 s29, s[14:15]
	v_cmp_le_u32_e64 s[34:35], s6, v126
	s_add_u32 s28, s28, s29
	v_addc_co_u32_e64 v8, s[20:21], 0, v8, s[8:9]
	s_bcnt1_i32_b64 s30, s[34:35]
	v_cmp_le_u32_e64 s[10:11], s6, v127
	s_add_u32 s28, s28, s30
	v_cmp_le_u32_e64 s[12:13], s6, v128
	s_bcnt1_i32_b64 s31, s[10:11]
	v_cmp_le_u32_e64 s[14:15], s6, v129
	s_add_u32 s28, s28, s31
	v_addc_co_u32_e64 v8, s[20:21], 0, v8, s[12:13]
	s_bcnt1_i32_b64 s29, s[14:15]
	v_cmp_le_u32_e64 s[16:17], s6, v130
	s_add_u32 s28, s28, s29
	v_cmp_le_u32_e64 s[34:35], s6, v132
	v_addc_co_u32_e64 v8, s[20:21], 0, v8, s[16:17]
	v_cmp_le_u32_e64 s[10:11], s6, v133
	s_bcnt1_i32_b64 s30, s[34:35]
	v_cmp_le_u32_e64 s[8:9], s6, v138
	s_add_u32 s28, s28, s30
	v_cmp_le_u32_e64 s[14:15], s6, v139
	s_bcnt1_i32_b64 s31, s[10:11]
	v_addc_co_u32_e64 v8, s[20:21], 0, v8, s[8:9]
	s_add_u32 s28, s28, s31
	v_cmp_le_u32_e64 s[12:13], s6, v141
	s_bcnt1_i32_b64 s29, s[14:15]
	v_cmp_le_u32_e64 s[34:35], s6, v143
	s_add_u32 s28, s28, s29
	v_addc_co_u32_e64 v8, s[20:21], 0, v8, s[12:13]
	s_bcnt1_i32_b64 s30, s[34:35]
	v_cmp_le_u32_e64 s[10:11], s6, v145
	s_add_u32 s28, s28, s30
	v_cmp_le_u32_e64 s[16:17], s6, v147
	s_bcnt1_i32_b64 s31, s[10:11]
	v_cmp_le_u32_e64 s[14:15], s6, v149
	s_add_u32 s28, s28, s31
	v_addc_co_u32_e64 v8, s[20:21], 0, v8, s[16:17]
	s_bcnt1_i32_b64 s29, s[14:15]
	v_cmp_le_u32_e64 s[8:9], s6, v151
	s_add_u32 s28, s28, s29
	s_nop 0
	v_addc_co_u32_e64 v8, s[20:21], 0, v8, s[8:9]
	v_and_b32_e32 v9, 8, v8
	v_cmp_ne_u32_e64 s[18:19], 0, v9
	v_and_b32_e32 v9, 4, v8
	v_cmp_ne_u32_e64 s[16:17], 0, v9
	v_and_b32_e32 v9, 2, v8
	v_cmp_ne_u32_e64 s[12:13], 0, v9
	v_and_b32_e32 v9, 1, v8
	v_cmp_ne_u32_e64 s[8:9], 0, v9
	s_bcnt1_i32_b64 s7, s[18:19]
	s_bcnt1_i32_b64 s3, s[16:17]
	s_lshl1_add_u32 s7, s7, s3
	s_bcnt1_i32_b64 s3, s[12:13]
	s_lshl1_add_u32 s7, s7, s3
	s_bcnt1_i32_b64 s3, s[8:9]
	s_lshl1_add_u32 s7, s7, s3
	s_add_u32 s7, s7, s28
	s_cmpk_lt_u32 s7, 0x100
	s_cselect_b32 s4, s4, s6
	s_cmpk_eq_u32 s7, 0x100
	s_cbranch_scc1 .Ltk2_x24
	s_lshr_b32 s5, s5, 1
	s_cbranch_scc1 .Ltk2_l24
	s_branch .Ltk2_orig
.Ltk2_l20:
	s_or_b32 s6, s4, s5
	v_cmp_le_u32_e64 s[10:11], s6, v111
	v_cmp_le_u32_e64 s[8:9], s6, v113
	v_cmp_le_u32_e64 s[14:15], s6, v115
	s_bcnt1_i32_b64 s28, s[10:11]
	v_cndmask_b32_e64 v8, 0, 1, s[8:9]
	s_bcnt1_i32_b64 s29, s[14:15]
	v_cmp_le_u32_e64 s[12:13], s6, v117
	s_add_u32 s28, s28, s29
	v_cmp_le_u32_e64 s[34:35], s6, v119
	v_addc_co_u32_e64 v8, s[20:21], 0, v8, s[12:13]
	v_cmp_le_u32_e64 s[10:11], s6, v121
	s_bcnt1_i32_b64 s30, s[34:35]
	v_cmp_le_u32_e64 s[16:17], s6, v123
	s_add_u32 s28, s28, s30
	v_cmp_le_u32_e64 s[14:15], s6, v124
	s_bcnt1_i32_b64 s31, s[10:11]
	v_addc_co_u32_e64 v8, s[20:21], 0, v8, s[16:17]
	s_add_u32 s28, s28, s31
	v_cmp_le_u32_e64 s[8:9], s6, v125
	s_bcnt1_i32_b64 s29, s[14:15]
	v_cmp_le_u32_e64 s[34:35], s6, v126
	s_add_u32 s28, s28, s29
	v_addc_co_u32_e64 v8, s[20:21], 0, v8, s[8:9]
	s_bcnt1_i32_b64 s30, s[34:35]
	v_cmp_le_u32_e64 s[10:11], s6, v127
	s_add_u32 s28, s28, s30
	v_cmp_le_u32_e64 s[12:13], s6, v128
	s_bcnt1_i32_b64 s31, s[10:11]
	v_cmp_le_u32_e64 s[14:15], s6, v129
	s_add_u32 s28, s28, s31
	v_addc_co_u32_e64 v8, s[20:21], 0, v8, s[12:13]
	s_bcnt1_i32_b64 s29, s[14:15]
	v_cmp_le_u32_e64 s[16:17], s6, v130
	s_add_u32 s28, s28, s29
	v_cmp_le_u32_e64 s[34:35], s6, v132
	v_addc_co_u32_e64 v8, s[20:21], 0, v8, s[16:17]
	v_cmp_le_u32_e64 s[10:11], s6, v133
	s_bcnt1_i32_b64 s30, s[34:35]
	v_cmp_le_u32_e64 s[8:9], s6, v138
	s_add_u32 s28, s28, s30
	v_cmp_le_u32_e64 s[14:15], s6, v139
	s_bcnt1_i32_b64 s31, s[10:11]
	v_addc_co_u32_e64 v8, s[20:21], 0, v8, s[8:9]
	s_add_u32 s28, s28, s31
	v_cmp_le_u32_e64 s[12:13], s6, v141
	s_bcnt1_i32_b64 s29, s[14:15]
	v_cmp_le_u32_e64 s[34:35], s6, v143
	s_add_u32 s28, s28, s29
	v_addc_co_u32_e64 v8, s[20:21], 0, v8, s[12:13]
	s_bcnt1_i32_b64 s30, s[34:35]
	s_add_u32 s28, s28, s30
	v_and_b32_e32 v9, 8, v8
	v_cmp_ne_u32_e64 s[18:19], 0, v9
	v_and_b32_e32 v9, 4, v8
	v_cmp_ne_u32_e64 s[16:17], 0, v9
	v_and_b32_e32 v9, 2, v8
	v_cmp_ne_u32_e64 s[12:13], 0, v9
	v_and_b32_e32 v9, 1, v8
	v_cmp_ne_u32_e64 s[8:9], 0, v9
	s_bcnt1_i32_b64 s7, s[18:19]
	s_bcnt1_i32_b64 s3, s[16:17]
	s_lshl1_add_u32 s7, s7, s3
	s_bcnt1_i32_b64 s3, s[12:13]
	s_lshl1_add_u32 s7, s7, s3
	s_bcnt1_i32_b64 s3, s[8:9]
	s_lshl1_add_u32 s7, s7, s3
	s_add_u32 s7, s7, s28
	s_cmpk_lt_u32 s7, 0x100
	s_cselect_b32 s4, s4, s6
	s_cmpk_eq_u32 s7, 0x100
	s_cbranch_scc1 .Ltk2_x20
	s_lshr_b32 s5, s5, 1
	s_cbranch_scc1 .Ltk2_l20
	s_branch .Ltk2_orig
.Ltk2_l16:
	s_or_b32 s6, s4, s5
	v_cmp_le_u32_e64 s[10:11], s6, v111
	v_cmp_le_u32_e64 s[8:9], s6, v113
	v_cmp_le_u32_e64 s[14:15], s6, v115
	s_bcnt1_i32_b64 s28, s[10:11]
	v_cndmask_b32_e64 v8, 0, 1, s[8:9]
	s_bcnt1_i32_b64 s29, s[14:15]
	v_cmp_le_u32_e64 s[12:13], s6, v117
	s_add_u32 s28, s28, s29
	v_cmp_le_u32_e64 s[34:35], s6, v119
	v_addc_co_u32_e64 v8, s[20:21], 0, v8, s[12:13]
	v_cmp_le_u32_e64 s[10:11], s6, v121
	s_bcnt1_i32_b64 s30, s[34:35]
	v_cmp_le_u32_e64 s[16:17], s6, v123
	s_add_u32 s28, s28, s30
	v_cmp_le_u32_e64 s[14:15], s6, v124
	s_bcnt1_i32_b64 s31, s[10:11]
	v_addc_co_u32_e64 v8, s[20:21], 0, v8, s[16:17]
	s_add_u32 s28, s28, s31
	v_cmp_le_u32_e64 s[8:9], s6, v125
	s_bcnt1_i32_b64 s29, s[14:15]
	v_cmp_le_u32_e64 s[34:35], s6, v126
	s_add_u32 s28, s28, s29
	v_addc_co_u32_e64 v8, s[20:21], 0, v8, s[8:9]
	s_bcnt1_i32_b64 s30, s[34:35]
	v_cmp_le_u32_e64 s[10:11], s6, v127
	s_add_u32 s28, s28, s30
	v_cmp_le_u32_e64 s[12:13], s6, v128
	s_bcnt1_i32_b64 s31, s[10:11]
	v_cmp_le_u32_e64 s[14:15], s6, v129
	s_add_u32 s28, s28, s31
	v_addc_co_u32_e64 v8, s[20:21], 0, v8, s[12:13]
	s_bcnt1_i32_b64 s29, s[14:15]
	v_cmp_le_u32_e64 s[16:17], s6, v130
	s_add_u32 s28, s28, s29
	v_cmp_le_u32_e64 s[34:35], s6, v132
	v_addc_co_u32_e64 v8, s[20:21], 0, v8, s[16:17]
	v_cmp_le_u32_e64 s[10:11], s6, v133
	s_bcnt1_i32_b64 s30, s[34:35]
	s_add_u32 s28, s28, s30
	s_bcnt1_i32_b64 s31, s[10:11]
	s_add_u32 s28, s28, s31
	v_and_b32_e32 v9, 4, v8
	v_cmp_ne_u32_e64 s[16:17], 0, v9
	v_and_b32_e32 v9, 2, v8
	v_cmp_ne_u32_e64 s[12:13], 0, v9
	v_and_b32_e32 v9, 1, v8
	v_cmp_ne_u32_e64 s[8:9], 0, v9
	s_bcnt1_i32_b64 s7, s[16:17]
	s_bcnt1_i32_b64 s3, s[12:13]
	s_lshl1_add_u32 s7, s7, s3
	s_bcnt1_i32_b64 s3, s[8:9]
	s_lshl1_add_u32 s7, s7, s3
	s_add_u32 s7, s7, s28
	s_cmpk_lt_u32 s7, 0x100
	s_cselect_b32 s4, s4, s6
	s_cmpk_eq_u32 s7, 0x100
	s_cbranch_scc1 .Ltk2_x16
	s_lshr_b32 s5, s5, 1
	s_cbranch_scc1 .Ltk2_l16
	s_branch .Ltk2_orig
.Ltk2_l12:
	s_or_b32 s6, s4, s5
	v_cmp_le_u32_e64 s[10:11], s6, v111
	v_cmp_le_u32_e64 s[8:9], s6, v113
	v_cmp_le_u32_e64 s[14:15], s6, v115
	s_bcnt1_i32_b64 s28, s[10:11]
	v_cndmask_b32_e64 v8, 0, 1, s[8:9]
	s_bcnt1_i32_b64 s29, s[14:15]
	v_cmp_le_u32_e64 s[12:13], s6, v117
	s_add_u32 s28, s28, s29
	v_cmp_le_u32_e64 s[34:35], s6, v119
	v_addc_co_u32_e64 v8, s[20:21], 0, v8, s[12:13]
	v_cmp_le_u32_e64 s[10:11], s6, v121
	s_bcnt1_i32_b64 s30, s[34:35]
	v_cmp_le_u32_e64 s[16:17], s6, v123
	s_add_u32 s28, s28, s30
	v_cmp_le_u32_e64 s[14:15], s6, v124
	s_bcnt1_i32_b64 s31, s[10:11]
	v_addc_co_u32_e64 v8, s[20:21], 0, v8, s[16:17]
	s_add_u32 s28, s28, s31
	v_cmp_le_u32_e64 s[8:9], s6, v125
	s_bcnt1_i32_b64 s29, s[14:15]
	v_cmp_le_u32_e64 s[34:35], s6, v126
	s_add_u32 s28, s28, s29
	v_addc_co_u32_e64 v8, s[20:21], 0, v8, s[8:9]
	s_bcnt1_i32_b64 s30, s[34:35]
	v_cmp_le_u32_e64 s[10:11], s6, v127
	s_add_u32 s28, s28, s30
	v_cmp_le_u32_e64 s[12:13], s6, v128
	s_bcnt1_i32_b64 s31, s[10:11]
	s_add_u32 s28, s28, s31
	v_addc_co_u32_e64 v8, s[20:21], 0, v8, s[12:13]
	v_and_b32_e32 v9, 4, v8
	v_cmp_ne_u32_e64 s[16:17], 0, v9
	v_and_b32_e32 v9, 2, v8
	v_cmp_ne_u32_e64 s[12:13], 0, v9
	v_and_b32_e32 v9, 1, v8
	v_cmp_ne_u32_e64 s[8:9], 0, v9
	s_bcnt1_i32_b64 s7, s[16:17]
	s_bcnt1_i32_b64 s3, s[12:13]
	s_lshl1_add_u32 s7, s7, s3
	s_bcnt1_i32_b64 s3, s[8:9]
	s_lshl1_add_u32 s7, s7, s3
	s_add_u32 s7, s7, s28
	s_cmpk_lt_u32 s7, 0x100
	s_cselect_b32 s4, s4, s6
	s_cmpk_eq_u32 s7, 0x100
	s_cbranch_scc1 .Ltk2_x12
	s_lshr_b32 s5, s5, 1
	s_cbranch_scc1 .Ltk2_l12
	s_branch .Ltk2_orig
.Ltk2_l8:
	s_or_b32 s6, s4, s5
	v_cmp_le_u32_e64 s[10:11], s6, v111
	v_cmp_le_u32_e64 s[8:9], s6, v113
	v_cmp_le_u32_e64 s[14:15], s6, v115
	s_bcnt1_i32_b64 s28, s[10:11]
	v_cndmask_b32_e64 v8, 0, 1, s[8:9]
	s_bcnt1_i32_b64 s29, s[14:15]
	v_cmp_le_u32_e64 s[12:13], s6, v117
	s_add_u32 s28, s28, s29
	v_cmp_le_u32_e64 s[34:35], s6, v119
	v_addc_co_u32_e64 v8, s[20:21], 0, v8, s[12:13]
	v_cmp_le_u32_e64 s[10:11], s6, v121
	s_bcnt1_i32_b64 s30, s[34:35]
	v_cmp_le_u32_e64 s[16:17], s6, v123
	s_add_u32 s28, s28, s30
	v_cmp_le_u32_e64 s[14:15], s6, v124
	s_bcnt1_i32_b64 s31, s[10:11]
	v_addc_co_u32_e64 v8, s[20:21], 0, v8, s[16:17]
	s_add_u32 s28, s28, s31
	s_bcnt1_i32_b64 s29, s[14:15]
	s_add_u32 s28, s28, s29
	v_and_b32_e32 v9, 2, v8
	v_cmp_ne_u32_e64 s[12:13], 0, v9
	v_and_b32_e32 v9, 1, v8
	v_cmp_ne_u32_e64 s[8:9], 0, v9
	s_bcnt1_i32_b64 s7, s[12:13]
	s_bcnt1_i32_b64 s3, s[8:9]
	s_lshl1_add_u32 s7, s7, s3
	s_add_u32 s7, s7, s28
	s_cmpk_lt_u32 s7, 0x100
	s_cselect_b32 s4, s4, s6
	s_cmpk_eq_u32 s7, 0x100
	s_cbranch_scc1 .Ltk2_x8
	s_lshr_b32 s5, s5, 1
	s_cbranch_scc1 .Ltk2_l8
	s_branch .Ltk2_orig

.Ltk3_l32:
	s_or_b32 s6, s4, s5
	v_cmp_le_u32_e64 s[10:11], s6, v93
	v_cmp_le_u32_e64 s[8:9], s6, v94
	v_cmp_le_u32_e64 s[14:15], s6, v95
	s_bcnt1_i32_b64 s28, s[10:11]
	v_cndmask_b32_e64 v8, 0, 1, s[8:9]
	s_bcnt1_i32_b64 s29, s[14:15]
	v_cmp_le_u32_e64 s[12:13], s6, v96
	s_add_u32 s28, s28, s29
	v_cmp_le_u32_e64 s[34:35], s6, v97
	v_addc_co_u32_e64 v8, s[20:21], 0, v8, s[12:13]
	v_cmp_le_u32_e64 s[10:11], s6, v98
	s_bcnt1_i32_b64 s30, s[34:35]
	v_cmp_le_u32_e64 s[16:17], s6, v99
	s_add_u32 s28, s28, s30
	v_cmp_le_u32_e64 s[14:15], s6, v100
	s_bcnt1_i32_b64 s31, s[10:11]
	v_addc_co_u32_e64 v8, s[20:21], 0, v8, s[16:17]
	s_add_u32 s28, s28, s31
	v_cmp_le_u32_e64 s[8:9], s6, v101
	s_bcnt1_i32_b64 s29, s[14:15]
	v_cmp_le_u32_e64 s[34:35], s6, v102
	s_add_u32 s28, s28, s29
	v_addc_co_u32_e64 v8, s[20:21], 0, v8, s[8:9]
	s_bcnt1_i32_b64 s30, s[34:35]
	v_cmp_le_u32_e64 s[10:11], s6, v103
	s_add_u32 s28, s28, s30
	v_cmp_le_u32_e64 s[12:13], s6, v104
	s_bcnt1_i32_b64 s31, s[10:11]
	v_cmp_le_u32_e64 s[14:15], s6, v105
	s_add_u32 s28, s28, s31
	v_addc_co_u32_e64 v8, s[20:21], 0, v8, s[12:13]
	s_bcnt1_i32_b64 s29, s[14:15]
	v_cmp_le_u32_e64 s[16:17], s6, v106
	s_add_u32 s28, s28, s29
	v_cmp_le_u32_e64 s[34:35], s6, v107
	v_addc_co_u32_e64 v8, s[20:21], 0, v8, s[16:17]
	v_cmp_le_u32_e64 s[10:11], s6, v108
	s_bcnt1_i32_b64 s30, s[34:35]
	v_cmp_le_u32_e64 s[8:9], s6, v109
	s_add_u32 s28, s28, s30
	v_cmp_le_u32_e64 s[14:15], s6, v110
	s_bcnt1_i32_b64 s31, s[10:11]
	v_addc_co_u32_e64 v8, s[20:21], 0, v8, s[8:9]
	s_add_u32 s28, s28, s31
	v_cmp_le_u32_e64 s[12:13], s6, v112
	s_bcnt1_i32_b64 s29, s[14:15]
	v_cmp_le_u32_e64 s[34:35], s6, v114
	s_add_u32 s28, s28, s29
	v_addc_co_u32_e64 v8, s[20:21], 0, v8, s[12:13]
	s_bcnt1_i32_b64 s30, s[34:35]
	v_cmp_le_u32_e64 s[10:11], s6, v116
	s_add_u32 s28, s28, s30
	v_cmp_le_u32_e64 s[16:17], s6, v118
	s_bcnt1_i32_b64 s31, s[10:11]
	v_cmp_le_u32_e64 s[14:15], s6, v120
	s_add_u32 s28, s28, s31
	v_addc_co_u32_e64 v8, s[20:21], 0, v8, s[16:17]
	s_bcnt1_i32_b64 s29, s[14:15]
	v_cmp_le_u32_e64 s[8:9], s6, v122
	s_add_u32 s28, s28, s29
	v_cmp_le_u32_e64 s[34:35], s6, v131
	v_addc_co_u32_e64 v8, s[20:21], 0, v8, s[8:9]
	v_cmp_le_u32_e64 s[10:11], s6, v90
	s_bcnt1_i32_b64 s30, s[34:35]
	v_cmp_le_u32_e64 s[12:13], s6, v91
	s_add_u32 s28, s28, s30
	v_cmp_le_u32_e64 s[14:15], s6, v134
	s_bcnt1_i32_b64 s31, s[10:11]
	v_addc_co_u32_e64 v8, s[20:21], 0, v8, s[12:13]
	s_add_u32 s28, s28, s31
	v_cmp_le_u32_e64 s[16:17], s6, v135
	s_bcnt1_i32_b64 s29, s[14:15]
	v_cmp_le_u32_e64 s[34:35], s6, v136
	s_add_u32 s28, s28, s29
	v_addc_co_u32_e64 v8, s[20:21], 0, v8, s[16:17]
	s_bcnt1_i32_b64 s30, s[34:35]
	v_cmp_le_u32_e64 s[10:11], s6, v137
	s_add_u32 s28, s28, s30
	v_cmp_le_u32_e64 s[8:9], s6, v4
	s_bcnt1_i32_b64 s31, s[10:11]
	s_add_u32 s28, s28, s31
	v_addc_co_u32_e64 v8, s[20:21], 0, v8, s[8:9]
	v_and_b32_e32 v9, 8, v8
	v_cmp_ne_u32_e64 s[18:19], 0, v9
	v_and_b32_e32 v9, 4, v8
	v_cmp_ne_u32_e64 s[16:17], 0, v9
	v_and_b32_e32 v9, 2, v8
	v_cmp_ne_u32_e64 s[12:13], 0, v9
	v_and_b32_e32 v9, 1, v8
	v_cmp_ne_u32_e64 s[8:9], 0, v9
	s_bcnt1_i32_b64 s7, s[18:19]
	s_bcnt1_i32_b64 s3, s[16:17]
	s_lshl1_add_u32 s7, s7, s3
	s_bcnt1_i32_b64 s3, s[12:13]
	s_lshl1_add_u32 s7, s7, s3
	s_bcnt1_i32_b64 s3, s[8:9]
	s_lshl1_add_u32 s7, s7, s3
	s_add_u32 s7, s7, s28
	s_cmpk_lt_u32 s7, 0x100
	s_cselect_b32 s4, s4, s6
	s_cmpk_eq_u32 s7, 0x100
	s_cbranch_scc1 .Ltk3_x32
	s_lshr_b32 s5, s5, 1
	s_cbranch_scc1 .Ltk3_l32
	s_branch .Ltk3_orig
.Ltk3_l28:
	s_or_b32 s6, s4, s5
	v_cmp_le_u32_e64 s[10:11], s6, v93
	v_cmp_le_u32_e64 s[8:9], s6, v94
	v_cmp_le_u32_e64 s[14:15], s6, v95
	s_bcnt1_i32_b64 s28, s[10:11]
	v_cndmask_b32_e64 v8, 0, 1, s[8:9]
	s_bcnt1_i32_b64 s29, s[14:15]
	v_cmp_le_u32_e64 s[12:13], s6, v96
	s_add_u32 s28, s28, s29
	v_cmp_le_u32_e64 s[34:35], s6, v97
	v_addc_co_u32_e64 v8, s[20:21], 0, v8, s[12:13]
	v_cmp_le_u32_e64 s[10:11], s6, v98
	s_bcnt1_i32_b64 s30, s[34:35]
	v_cmp_le_u32_e64 s[16:17], s6, v99
	s_add_u32 s28, s28, s30
	v_cmp_le_u32_e64 s[14:15], s6, v100
	s_bcnt1_i32_b64 s31, s[10:11]
	v_addc_co_u32_e64 v8, s[20:21], 0, v8, s[16:17]
	s_add_u32 s28, s28, s31
	v_cmp_le_u32_e64 s[8:9], s6, v101
	s_bcnt1_i32_b64 s29, s[14:15]
	v_cmp_le_u32_e64 s[34:35], s6, v102
	s_add_u32 s28, s28, s29
	v_addc_co_u32_e64 v8, s[20:21], 0, v8, s[8:9]
	s_bcnt1_i32_b64 s30, s[34:35]
	v_cmp_le_u32_e64 s[10:11], s6, v103
	s_add_u32 s28, s28, s30
	v_cmp_le_u32_e64 s[12:13], s6, v104
	s_bcnt1_i32_b64 s31, s[10:11]
	v_cmp_le_u32_e64 s[14:15], s6, v105
	s_add_u32 s28, s28, s31
	v_addc_co_u32_e64 v8, s[20:21], 0, v8, s[12:13]
	s_bcnt1_i32_b64 s29, s[14:15]
	v_cmp_le_u32_e64 s[16:17], s6, v106
	s_add_u32 s28, s28, s29
	v_cmp_le_u32_e64 s[34:35], s6, v107
	v_addc_co_u32_e64 v8, s[20:21], 0, v8, s[16:17]
	v_cmp_le_u32_e64 s[10:11], s6, v108
	s_bcnt1_i32_b64 s30, s[34:35]
	v_cmp_le_u32_e64 s[8:9], s6, v109
	s_add_u32 s28, s28, s30
	v_cmp_le_u32_e64 s[14:15], s6, v110
	s_bcnt1_i32_b64 s31, s[10:11]
	v_addc_co_u32_e64 v8, s[20:21], 0, v8, s[8:9]
	s_add_u32 s28, s28, s31
	v_cmp_le_u32_e64 s[12:13], s6, v112
	s_bcnt1_i32_b64 s29, s[14:15]
	v_cmp_le_u32_e64 s[34:35], s6, v114
	s_add_u32 s28, s28, s29
	v_addc_co_u32_e64 v8, s[20:21], 0, v8, s[12:13]
	s_bcnt1_i32_b64 s30, s[34:35]
	v_cmp_le_u32_e64 s[10:11], s6, v116
	s_add_u32 s28, s28, s30
	v_cmp_le_u32_e64 s[16:17], s6, v118
	s_bcnt1_i32_b64 s31, s[10:11]
	v_cmp_le_u32_e64 s[14:15], s6, v120
	s_add_u32 s28, s28, s31
	v_addc_co_u32_e64 v8, s[20:21], 0, v8, s[16:17]
	s_bcnt1_i32_b64 s29, s[14:15]
	v_cmp_le_u32_e64 s[8:9], s6, v122
	s_add_u32 s28, s28, s29
	v_cmp_le_u32_e64 s[34:35], s6, v131
	v_addc_co_u32_e64 v8, s[20:21], 0, v8, s[8:9]
	v_cmp_le_u32_e64 s[10:11], s6, v90
	s_bcnt1_i32_b64 s30, s[34:35]
	v_cmp_le_u32_e64 s[12:13], s6, v91
	s_add_u32 s28, s28, s30
	v_cmp_le_u32_e64 s[14:15], s6, v134
	s_bcnt1_i32_b64 s31, s[10:11]
	v_addc_co_u32_e64 v8, s[20:21], 0, v8, s[12:13]
	s_add_u32 s28, s28, s31
	s_bcnt1_i32_b64 s29, s[14:15]
	s_add_u32 s28, s28, s29
	v_and_b32_e32 v9, 8, v8
	v_cmp_ne_u32_e64 s[18:19], 0, v9
	v_and_b32_e32 v9, 4, v8
	v_cmp_ne_u32_e64 s[16:17], 0, v9
	v_and_b32_e32 v9, 2, v8
	v_cmp_ne_u32_e64 s[12:13], 0, v9
	v_and_b32_e32 v9, 1, v8
	v_cmp_ne_u32_e64 s[8:9], 0, v9
	s_bcnt1_i32_b64 s7, s[18:19]
	s_bcnt1_i32_b64 s3, s[16:17]
	s_lshl1_add_u32 s7, s7, s3
	s_bcnt1_i32_b64 s3, s[12:13]
	s_lshl1_add_u32 s7, s7, s3
	s_bcnt1_i32_b64 s3, s[8:9]
	s_lshl1_add_u32 s7, s7, s3
	s_add_u32 s7, s7, s28
	s_cmpk_lt_u32 s7, 0x100
	s_cselect_b32 s4, s4, s6
	s_cmpk_eq_u32 s7, 0x100
	s_cbranch_scc1 .Ltk3_x28
	s_lshr_b32 s5, s5, 1
	s_cbranch_scc1 .Ltk3_l28
	s_branch .Ltk3_orig
.Ltk3_l24:
	s_or_b32 s6, s4, s5
	v_cmp_le_u32_e64 s[10:11], s6, v93
	v_cmp_le_u32_e64 s[8:9], s6, v94
	v_cmp_le_u32_e64 s[14:15], s6, v95
	s_bcnt1_i32_b64 s28, s[10:11]
	v_cndmask_b32_e64 v8, 0, 1, s[8:9]
	s_bcnt1_i32_b64 s29, s[14:15]
	v_cmp_le_u32_e64 s[12:13], s6, v96
	s_add_u32 s28, s28, s29
	v_cmp_le_u32_e64 s[34:35], s6, v97
	v_addc_co_u32_e64 v8, s[20:21], 0, v8, s[12:13]
	v_cmp_le_u32_e64 s[10:11], s6, v98
	s_bcnt1_i32_b64 s30, s[34:35]
	v_cmp_le_u32_e64 s[16:17], s6, v99
	s_add_u32 s28, s28, s30
	v_cmp_le_u32_e64 s[14:15], s6, v100
	s_bcnt1_i32_b64 s31, s[10:11]
	v_addc_co_u32_e64 v8, s[20:21], 0, v8, s[16:17]
	s_add_u32 s28, s28, s31
	v_cmp_le_u32_e64 s[8:9], s6, v101
	s_bcnt1_i32_b64 s29, s[14:15]
	v_cmp_le_u32_e64 s[34:35], s6, v102
	s_add_u32 s28, s28, s29
	v_addc_co_u32_e64 v8, s[20:21], 0, v8, s[8:9]
	s_bcnt1_i32_b64 s30, s[34:35]
	v_cmp_le_u32_e64 s[10:11], s6, v103
	s_add_u32 s28, s28, s30
	v_cmp_le_u32_e64 s[12:13], s6, v104
	s_bcnt1_i32_b64 s31, s[10:11]
	v_cmp_le_u32_e64 s[14:15], s6, v105
	s_add_u32 s28, s28, s31
	v_addc_co_u32_e64 v8, s[20:21], 0, v8, s[12:13]
	s_bcnt1_i32_b64 s29, s[14:15]
	v_cmp_le_u32_e64 s[16:17], s6, v106
	s_add_u32 s28, s28, s29
	v_cmp_le_u32_e64 s[34:35], s6, v107
	v_addc_co_u32_e64 v8, s[20:21], 0, v8, s[16:17]
	v_cmp_le_u32_e64 s[10:11], s6, v108
	s_bcnt1_i32_b64 s30, s[34:35]
	v_cmp_le_u32_e64 s[8:9], s6, v109
	s_add_u32 s28, s28, s30
	v_cmp_le_u32_e64 s[14:15], s6, v110
	s_bcnt1_i32_b64 s31, s[10:11]
	v_addc_co_u32_e64 v8, s[20:21], 0, v8, s[8:9]
	s_add_u32 s28, s28, s31
	v_cmp_le_u32_e64 s[12:13], s6, v112
	s_bcnt1_i32_b64 s29, s[14:15]
	v_cmp_le_u32_e64 s[34:35], s6, v114
	s_add_u32 s28, s28, s29
	v_addc_co_u32_e64 v8, s[20:21], 0, v8, s[12:13]
	s_bcnt1_i32_b64 s30, s[34:35]
	v_cmp_le_u32_e64 s[10:11], s6, v116
	s_add_u32 s28, s28, s30
	v_cmp_le_u32_e64 s[16:17], s6, v118
	s_bcnt1_i32_b64 s31, s[10:11]
	v_cmp_le_u32_e64 s[14:15], s6, v120
	s_add_u32 s28, s28, s31
	v_addc_co_u32_e64 v8, s[20:21], 0, v8, s[16:17]
	s_bcnt1_i32_b64 s29, s[14:15]
	v_cmp_le_u32_e64 s[8:9], s6, v122
	s_add_u32 s28, s28, s29
	s_nop 0
	v_addc_co_u32_e64 v8, s[20:21], 0, v8, s[8:9]
	v_and_b32_e32 v9, 8, v8
	v_cmp_ne_u32_e64 s[18:19], 0, v9
	v_and_b32_e32 v9, 4, v8
	v_cmp_ne_u32_e64 s[16:17], 0, v9
	v_and_b32_e32 v9, 2, v8
	v_cmp_ne_u32_e64 s[12:13], 0, v9
	v_and_b32_e32 v9, 1, v8
	v_cmp_ne_u32_e64 s[8:9], 0, v9
	s_bcnt1_i32_b64 s7, s[18:19]
	s_bcnt1_i32_b64 s3, s[16:17]
	s_lshl1_add_u32 s7, s7, s3
	s_bcnt1_i32_b64 s3, s[12:13]
	s_lshl1_add_u32 s7, s7, s3
	s_bcnt1_i32_b64 s3, s[8:9]
	s_lshl1_add_u32 s7, s7, s3
	s_add_u32 s7, s7, s28
	s_cmpk_lt_u32 s7, 0x100
	s_cselect_b32 s4, s4, s6
	s_cmpk_eq_u32 s7, 0x100
	s_cbranch_scc1 .Ltk3_x24
	s_lshr_b32 s5, s5, 1
	s_cbranch_scc1 .Ltk3_l24
	s_branch .Ltk3_orig
.Ltk3_l20:
	s_or_b32 s6, s4, s5
	v_cmp_le_u32_e64 s[10:11], s6, v93
	v_cmp_le_u32_e64 s[8:9], s6, v94
	v_cmp_le_u32_e64 s[14:15], s6, v95
	s_bcnt1_i32_b64 s28, s[10:11]
	v_cndmask_b32_e64 v8, 0, 1, s[8:9]
	s_bcnt1_i32_b64 s29, s[14:15]
	v_cmp_le_u32_e64 s[12:13], s6, v96
	s_add_u32 s28, s28, s29
	v_cmp_le_u32_e64 s[34:35], s6, v97
	v_addc_co_u32_e64 v8, s[20:21], 0, v8, s[12:13]
	v_cmp_le_u32_e64 s[10:11], s6, v98
	s_bcnt1_i32_b64 s30, s[34:35]
	v_cmp_le_u32_e64 s[16:17], s6, v99
	s_add_u32 s28, s28, s30
	v_cmp_le_u32_e64 s[14:15], s6, v100
	s_bcnt1_i32_b64 s31, s[10:11]
	v_addc_co_u32_e64 v8, s[20:21], 0, v8, s[16:17]
	s_add_u32 s28, s28, s31
	v_cmp_le_u32_e64 s[8:9], s6, v101
	s_bcnt1_i32_b64 s29, s[14:15]
	v_cmp_le_u32_e64 s[34:35], s6, v102
	s_add_u32 s28, s28, s29
	v_addc_co_u32_e64 v8, s[20:21], 0, v8, s[8:9]
	s_bcnt1_i32_b64 s30, s[34:35]
	v_cmp_le_u32_e64 s[10:11], s6, v103
	s_add_u32 s28, s28, s30
	v_cmp_le_u32_e64 s[12:13], s6, v104
	s_bcnt1_i32_b64 s31, s[10:11]
	v_cmp_le_u32_e64 s[14:15], s6, v105
	s_add_u32 s28, s28, s31
	v_addc_co_u32_e64 v8, s[20:21], 0, v8, s[12:13]
	s_bcnt1_i32_b64 s29, s[14:15]
	v_cmp_le_u32_e64 s[16:17], s6, v106
	s_add_u32 s28, s28, s29
	v_cmp_le_u32_e64 s[34:35], s6, v107
	v_addc_co_u32_e64 v8, s[20:21], 0, v8, s[16:17]
	v_cmp_le_u32_e64 s[10:11], s6, v108
	s_bcnt1_i32_b64 s30, s[34:35]
	v_cmp_le_u32_e64 s[8:9], s6, v109
	s_add_u32 s28, s28, s30
	v_cmp_le_u32_e64 s[14:15], s6, v110
	s_bcnt1_i32_b64 s31, s[10:11]
	v_addc_co_u32_e64 v8, s[20:21], 0, v8, s[8:9]
	s_add_u32 s28, s28, s31
	v_cmp_le_u32_e64 s[12:13], s6, v112
	s_bcnt1_i32_b64 s29, s[14:15]
	v_cmp_le_u32_e64 s[34:35], s6, v114
	s_add_u32 s28, s28, s29
	v_addc_co_u32_e64 v8, s[20:21], 0, v8, s[12:13]
	s_bcnt1_i32_b64 s30, s[34:35]
	s_add_u32 s28, s28, s30
	v_and_b32_e32 v9, 8, v8
	v_cmp_ne_u32_e64 s[18:19], 0, v9
	v_and_b32_e32 v9, 4, v8
	v_cmp_ne_u32_e64 s[16:17], 0, v9
	v_and_b32_e32 v9, 2, v8
	v_cmp_ne_u32_e64 s[12:13], 0, v9
	v_and_b32_e32 v9, 1, v8
	v_cmp_ne_u32_e64 s[8:9], 0, v9
	s_bcnt1_i32_b64 s7, s[18:19]
	s_bcnt1_i32_b64 s3, s[16:17]
	s_lshl1_add_u32 s7, s7, s3
	s_bcnt1_i32_b64 s3, s[12:13]
	s_lshl1_add_u32 s7, s7, s3
	s_bcnt1_i32_b64 s3, s[8:9]
	s_lshl1_add_u32 s7, s7, s3
	s_add_u32 s7, s7, s28
	s_cmpk_lt_u32 s7, 0x100
	s_cselect_b32 s4, s4, s6
	s_cmpk_eq_u32 s7, 0x100
	s_cbranch_scc1 .Ltk3_x20
	s_lshr_b32 s5, s5, 1
	s_cbranch_scc1 .Ltk3_l20
	s_branch .Ltk3_orig
.Ltk3_l16:
	s_or_b32 s6, s4, s5
	v_cmp_le_u32_e64 s[10:11], s6, v93
	v_cmp_le_u32_e64 s[8:9], s6, v94
	v_cmp_le_u32_e64 s[14:15], s6, v95
	s_bcnt1_i32_b64 s28, s[10:11]
	v_cndmask_b32_e64 v8, 0, 1, s[8:9]
	s_bcnt1_i32_b64 s29, s[14:15]
	v_cmp_le_u32_e64 s[12:13], s6, v96
	s_add_u32 s28, s28, s29
	v_cmp_le_u32_e64 s[34:35], s6, v97
	v_addc_co_u32_e64 v8, s[20:21], 0, v8, s[12:13]
	v_cmp_le_u32_e64 s[10:11], s6, v98
	s_bcnt1_i32_b64 s30, s[34:35]
	v_cmp_le_u32_e64 s[16:17], s6, v99
	s_add_u32 s28, s28, s30
	v_cmp_le_u32_e64 s[14:15], s6, v100
	s_bcnt1_i32_b64 s31, s[10:11]
	v_addc_co_u32_e64 v8, s[20:21], 0, v8, s[16:17]
	s_add_u32 s28, s28, s31
	v_cmp_le_u32_e64 s[8:9], s6, v101
	s_bcnt1_i32_b64 s29, s[14:15]
	v_cmp_le_u32_e64 s[34:35], s6, v102
	s_add_u32 s28, s28, s29
	v_addc_co_u32_e64 v8, s[20:21], 0, v8, s[8:9]
	s_bcnt1_i32_b64 s30, s[34:35]
	v_cmp_le_u32_e64 s[10:11], s6, v103
	s_add_u32 s28, s28, s30
	v_cmp_le_u32_e64 s[12:13], s6, v104
	s_bcnt1_i32_b64 s31, s[10:11]
	v_cmp_le_u32_e64 s[14:15], s6, v105
	s_add_u32 s28, s28, s31
	v_addc_co_u32_e64 v8, s[20:21], 0, v8, s[12:13]
	s_bcnt1_i32_b64 s29, s[14:15]
	v_cmp_le_u32_e64 s[16:17], s6, v106
	s_add_u32 s28, s28, s29
	v_cmp_le_u32_e64 s[34:35], s6, v107
	v_addc_co_u32_e64 v8, s[20:21], 0, v8, s[16:17]
	v_cmp_le_u32_e64 s[10:11], s6, v108
	s_bcnt1_i32_b64 s30, s[34:35]
	s_add_u32 s28, s28, s30
	s_bcnt1_i32_b64 s31, s[10:11]
	s_add_u32 s28, s28, s31
	v_and_b32_e32 v9, 4, v8
	v_cmp_ne_u32_e64 s[16:17], 0, v9
	v_and_b32_e32 v9, 2, v8
	v_cmp_ne_u32_e64 s[12:13], 0, v9
	v_and_b32_e32 v9, 1, v8
	v_cmp_ne_u32_e64 s[8:9], 0, v9
	s_bcnt1_i32_b64 s7, s[16:17]
	s_bcnt1_i32_b64 s3, s[12:13]
	s_lshl1_add_u32 s7, s7, s3
	s_bcnt1_i32_b64 s3, s[8:9]
	s_lshl1_add_u32 s7, s7, s3
	s_add_u32 s7, s7, s28
	s_cmpk_lt_u32 s7, 0x100
	s_cselect_b32 s4, s4, s6
	s_cmpk_eq_u32 s7, 0x100
	s_cbranch_scc1 .Ltk3_x16
	s_lshr_b32 s5, s5, 1
	s_cbranch_scc1 .Ltk3_l16
	s_branch .Ltk3_orig
.Ltk3_l12:
	s_or_b32 s6, s4, s5
	v_cmp_le_u32_e64 s[10:11], s6, v93
	v_cmp_le_u32_e64 s[8:9], s6, v94
	v_cmp_le_u32_e64 s[14:15], s6, v95
	s_bcnt1_i32_b64 s28, s[10:11]
	v_cndmask_b32_e64 v8, 0, 1, s[8:9]
	s_bcnt1_i32_b64 s29, s[14:15]
	v_cmp_le_u32_e64 s[12:13], s6, v96
	s_add_u32 s28, s28, s29
	v_cmp_le_u32_e64 s[34:35], s6, v97
	v_addc_co_u32_e64 v8, s[20:21], 0, v8, s[12:13]
	v_cmp_le_u32_e64 s[10:11], s6, v98
	s_bcnt1_i32_b64 s30, s[34:35]
	v_cmp_le_u32_e64 s[16:17], s6, v99
	s_add_u32 s28, s28, s30
	v_cmp_le_u32_e64 s[14:15], s6, v100
	s_bcnt1_i32_b64 s31, s[10:11]
	v_addc_co_u32_e64 v8, s[20:21], 0, v8, s[16:17]
	s_add_u32 s28, s28, s31
	v_cmp_le_u32_e64 s[8:9], s6, v101
	s_bcnt1_i32_b64 s29, s[14:15]
	v_cmp_le_u32_e64 s[34:35], s6, v102
	s_add_u32 s28, s28, s29
	v_addc_co_u32_e64 v8, s[20:21], 0, v8, s[8:9]
	s_bcnt1_i32_b64 s30, s[34:35]
	v_cmp_le_u32_e64 s[10:11], s6, v103
	s_add_u32 s28, s28, s30
	v_cmp_le_u32_e64 s[12:13], s6, v104
	s_bcnt1_i32_b64 s31, s[10:11]
	s_add_u32 s28, s28, s31
	v_addc_co_u32_e64 v8, s[20:21], 0, v8, s[12:13]
	v_and_b32_e32 v9, 4, v8
	v_cmp_ne_u32_e64 s[16:17], 0, v9
	v_and_b32_e32 v9, 2, v8
	v_cmp_ne_u32_e64 s[12:13], 0, v9
	v_and_b32_e32 v9, 1, v8
	v_cmp_ne_u32_e64 s[8:9], 0, v9
	s_bcnt1_i32_b64 s7, s[16:17]
	s_bcnt1_i32_b64 s3, s[12:13]
	s_lshl1_add_u32 s7, s7, s3
	s_bcnt1_i32_b64 s3, s[8:9]
	s_lshl1_add_u32 s7, s7, s3
	s_add_u32 s7, s7, s28
	s_cmpk_lt_u32 s7, 0x100
	s_cselect_b32 s4, s4, s6
	s_cmpk_eq_u32 s7, 0x100
	s_cbranch_scc1 .Ltk3_x12
	s_lshr_b32 s5, s5, 1
	s_cbranch_scc1 .Ltk3_l12
	s_branch .Ltk3_orig
.Ltk3_l8:
	s_or_b32 s6, s4, s5
	v_cmp_le_u32_e64 s[10:11], s6, v93
	v_cmp_le_u32_e64 s[8:9], s6, v94
	v_cmp_le_u32_e64 s[14:15], s6, v95
	s_bcnt1_i32_b64 s28, s[10:11]
	v_cndmask_b32_e64 v8, 0, 1, s[8:9]
	s_bcnt1_i32_b64 s29, s[14:15]
	v_cmp_le_u32_e64 s[12:13], s6, v96
	s_add_u32 s28, s28, s29
	v_cmp_le_u32_e64 s[34:35], s6, v97
	v_addc_co_u32_e64 v8, s[20:21], 0, v8, s[12:13]
	v_cmp_le_u32_e64 s[10:11], s6, v98
	s_bcnt1_i32_b64 s30, s[34:35]
	v_cmp_le_u32_e64 s[16:17], s6, v99
	s_add_u32 s28, s28, s30
	v_cmp_le_u32_e64 s[14:15], s6, v100
	s_bcnt1_i32_b64 s31, s[10:11]
	v_addc_co_u32_e64 v8, s[20:21], 0, v8, s[16:17]
	s_add_u32 s28, s28, s31
	s_bcnt1_i32_b64 s29, s[14:15]
	s_add_u32 s28, s28, s29
	v_and_b32_e32 v9, 2, v8
	v_cmp_ne_u32_e64 s[12:13], 0, v9
	v_and_b32_e32 v9, 1, v8
	v_cmp_ne_u32_e64 s[8:9], 0, v9
	s_bcnt1_i32_b64 s7, s[12:13]
	s_bcnt1_i32_b64 s3, s[8:9]
	s_lshl1_add_u32 s7, s7, s3
	s_add_u32 s7, s7, s28
	s_cmpk_lt_u32 s7, 0x100
	s_cselect_b32 s4, s4, s6
	s_cmpk_eq_u32 s7, 0x100
	s_cbranch_scc1 .Ltk3_x8
	s_lshr_b32 s5, s5, 1
	s_cbranch_scc1 .Ltk3_l8
	s_branch .Ltk3_orig
